# stack 2: K-loop back-edge bookkeeping inside the last MFMA block (6 loops), scatter-epilogue canonicalize removal, gain preheader waits dropped (in-order counted waits cover them)
# baseline (speedup 1.0000x reference)
; #define GAS __attribute__((address_space(1)))
; template <int MODE, bool W8 = false>
; __device__ __forceinline__ void norm_rows(const Ctx& C, const void* src, bf16* xdst, const unsigned char* YS8, const int* srow, const float* gate, const float* gain, bf16* XN, float* outf, unsigned char* XN8 = nullptr) {
;     ...
;     for (int m0 = C.gw; m0 < T; m0 += NR * C.NGW) {
;         f32x4 v[NR][8]; unsigned ya[NR][8], yb[NR][8]; float h0[NR], h1[NR];
; #pragma unroll
;         for (int q = 0; q < NR; ++q) { const int m = m0 + q * C.NGW;
;             if (MODE == 0) { const GAS f32x4* xr = (const GAS f32x4*)((const float*)src + (size_t)m * DM) + C.lane;
; #pragma unroll
;                 for (int j = 0; j < 8; ++j) v[q][j] = xr[64 * j]; }
;             else { const GAS v2u* xr = (const GAS v2u*)((const bf16*)src + (size_t)m * DM) + C.lane;
; #pragma unroll
;                 for (int j = 0; j < 8; ++j) { const v2u t_ = xr[64 * j]; v[q][j] = (f32x4){bflo(t_.x), bfhi(t_.x), bflo(t_.y), bfhi(t_.y)}; } }
;             if (MODE >= 1) {
;                 h0[q] = gate[2 * m] * (1.0f / SY); h1[q] = gate[2 * m + 1] * (1.0f / SY);
;                 const GAS unsigned* y0 = (const GAS unsigned*)(YS8 + (size_t)srow[2 * m] * DM) + C.lane; const GAS unsigned* y1 = (const GAS unsigned*)(YS8 + (size_t)srow[2 * m + 1] * DM) + C.lane;
; #pragma unroll
;                 for (int j = 0; j < 8; ++j) { ya[q][j] = y0[64 * j]; yb[q][j] = y1[64 * j]; } } }
; #pragma unroll
;         for (int q = 0; q < NR; ++q) { const int m = m0 + q * C.NGW;
;             if (MODE >= 1) {
; #pragma unroll
;                 for (int j = 0; j < 8; ++j) { const unsigned a = ya[q][j], b = yb[q][j];
;                     const f32x2_m a01 = __builtin_amdgcn_cvt_pk_f32_fp8((int)a, false), a23 = __builtin_amdgcn_cvt_pk_f32_fp8((int)a, true), b01 = __builtin_amdgcn_cvt_pk_f32_fp8((int)b, false), b23 = __builtin_amdgcn_cvt_pk_f32_fp8((int)b, true);
;                     v[q][j].x += h0[q] * a01.x + h1[q] * b01.x; v[q][j].y += h0[q] * a01.y + h1[q] * b01.y; v[q][j].z += h0[q] * a23.x + h1[q] * b23.x; v[q][j].w += h0[q] * a23.y + h1[q] * b23.y; } }
;             float ss = 0.f;
; #pragma unroll
;             for (int j = 0; j < 8; ++j) ss += (v[q][j].x * v[q][j].x + v[q][j].y * v[q][j].y) + (v[q][j].z * v[q][j].z + v[q][j].w * v[q][j].w);
;             const float rstd = 1.0f / sqrtf(wave_sum(ss) * (1.0f / DM) + RMS_EPS);
.LBB0_120:
	s_or_b64 exec, exec, s[12:13]
	s_cmpk_gt_i32 s16, 0x3fff
	s_cbranch_scc1 .LBB0_123
	v_mbcnt_lo_u32_b32 v2, -1, 0
	s_load_dwordx2 s[2:3], s[20:21], 0x10
	v_mbcnt_hi_u32_b32 v2, -1, v2
	v_and_b32_e32 v3, 64, v2
	v_add_u32_e32 v3, 64, v3
	v_xor_b32_e32 v4, 1, v2
	v_ashrrev_i32_e32 v1, 31, v0
	v_cmp_lt_i32_e32 vcc, v4, v3
	s_waitcnt vmcnt(24)
	v_lshlrev_b64 v[56:57], 4, v[0:1]
	s_waitcnt vmcnt(22) lgkmcnt(0)
	v_lshl_add_u64 v[58:59], s[2:3], 0, v[56:57]
	v_cndmask_b32_e32 v4, v2, v4, vcc
	s_waitcnt vmcnt(8)
	v_lshlrev_b32_e32 v73, 2, v4
	v_xor_b32_e32 v4, 2, v2
	s_mov_b64 s[2:3], 0x1000
	v_cmp_lt_i32_e32 vcc, v4, v3
	v_lshl_add_u64 v[60:61], v[58:59], 0, s[2:3]
	s_mov_b64 s[2:3], 0x1400
	v_cndmask_b32_e32 v4, v2, v4, vcc
	v_lshl_add_u64 v[62:63], v[58:59], 0, s[2:3]
	s_mov_b64 s[2:3], 0x1800
	s_waitcnt vmcnt(7)
	v_lshlrev_b32_e32 v74, 2, v4
	v_xor_b32_e32 v4, 4, v2
	v_lshl_add_u64 v[64:65], v[58:59], 0, s[2:3]
	s_mov_b64 s[2:3], 0x1c00
	v_cmp_lt_i32_e32 vcc, v4, v3
	v_lshl_add_u64 v[66:67], v[58:59], 0, s[2:3]
	s_add_i32 s2, s16, 0x800
	v_cndmask_b32_e32 v4, v2, v4, vcc
	s_ashr_i32 s3, s2, 31
	s_waitcnt vmcnt(6)
	v_lshlrev_b32_e32 v75, 2, v4
	v_xor_b32_e32 v4, 8, v2
	s_add_i32 s12, s16, 0xfffff000
	s_lshl_b64 s[4:5], s[2:3], 12
	v_cmp_lt_i32_e32 vcc, v4, v3
	s_add_u32 s4, s18, s4
	s_addc_u32 s5, s19, s5
	v_cndmask_b32_e32 v4, v2, v4, vcc
	s_lshl_b64 s[2:3], s[2:3], 13
	s_waitcnt vmcnt(5)
	v_lshlrev_b32_e32 v76, 2, v4
	v_xor_b32_e32 v4, 16, v2
	s_add_u32 s6, s8, s2
	v_cmp_lt_i32_e32 vcc, v4, v3
	s_addc_u32 s7, s9, s3
	s_ashr_i32 s17, s16, 31
	v_cndmask_b32_e32 v4, v2, v4, vcc
	s_lshl_b64 s[2:3], s[16:17], 13
	s_waitcnt vmcnt(4)
	v_lshlrev_b32_e32 v77, 2, v4
	v_xor_b32_e32 v4, 32, v2
	s_add_u32 s8, s8, s2
	v_cmp_lt_i32_e32 vcc, v4, v3
	s_addc_u32 s9, s9, s3
	s_lshl_b64 s[2:3], s[16:17], 12
	v_cndmask_b32_e32 v2, v2, v4, vcc
	s_add_u32 s10, s18, s2
	v_lshlrev_b32_e32 v78, 2, v2
	v_lshlrev_b64 v[68:69], 3, v[0:1]
	s_addc_u32 s11, s19, s3
	s_movk_i32 s13, 0x1000
	v_mov_b32_e32 v79, 0x358637bd
	s_mov_b32 s14, 0xf800000
	v_mov_b32_e32 v80, 0x260
	s_brev_b32 s15, 44
	global_load_dwordx4 v[160:163], v[58:59], off
	global_load_dwordx4 v[164:167], v[58:59], off offset:1024
	global_load_dwordx4 v[168:171], v[58:59], off offset:2048
	global_load_dwordx4 v[172:175], v[58:59], off offset:3072
	global_load_dwordx4 v[176:179], v[60:61], off
	global_load_dwordx4 v[180:183], v[62:63], off
	global_load_dwordx4 v[184:187], v[64:65], off
	global_load_dwordx4 v[188:191], v[66:67], off
.LBB0_122:
	v_lshl_add_u64 v[16:17], s[8:9], 0, v[56:57]
	global_load_dwordx4 v[86:89], v[16:17], off
	global_load_dwordx4 v[90:93], v[16:17], off offset:1024
	global_load_dwordx4 v[52:55], v[16:17], off offset:2048
	global_load_dwordx4 v[44:47], v[16:17], off offset:3072
	v_add_co_u32_e32 v16, vcc, 0x1000, v16
	v_lshl_add_u64 v[18:19], s[6:7], 0, v[56:57]
	s_nop 0
	v_addc_co_u32_e32 v17, vcc, 0, v17, vcc
	global_load_dwordx4 v[12:15], v[18:19], off
	global_load_dwordx4 v[8:11], v[18:19], off offset:1024
	global_load_dwordx4 v[4:7], v[18:19], off offset:2048
	global_load_dwordx4 v[0:3], v[18:19], off offset:3072
	global_load_dwordx4 v[40:43], v[16:17], off offset:1024
	global_load_dwordx4 v[48:51], v[16:17], off
	global_load_dwordx4 v[32:35], v[16:17], off offset:3072
	global_load_dwordx4 v[36:39], v[16:17], off offset:2048
	v_lshl_add_u64 v[20:21], s[10:11], 0, v[68:69]
	v_add_co_u32_e32 v94, vcc, s13, v18
	v_add_co_u32_e64 v70, s[2:3], s15, v20
	s_nop 0
	v_addc_co_u32_e32 v95, vcc, 0, v19, vcc
	v_addc_co_u32_e64 v71, s[2:3], 0, v21, s[2:3]
	global_load_dwordx4 v[24:27], v[94:95], off
	global_load_dwordx4 v[20:23], v[94:95], off offset:1024
	global_load_dwordx4 v[28:31], v[94:95], off offset:2048
	global_load_dwordx4 v[16:19], v[94:95], off offset:3072
	s_addk_i32 s12, 0x1000
	s_waitcnt vmcnt(15)
	v_mov_b32_e32 v96, v87
	s_waitcnt vmcnt(14)
	v_mov_b32_e32 v97, v91
	v_mov_b32_e32 v100, v89
	v_mov_b32_e32 v101, v93
	v_mov_b32_e32 v94, v86
	v_mov_b32_e32 v95, v90
	v_mov_b32_e32 v98, v88
	v_mov_b32_e32 v99, v92
	s_waitcnt vmcnt(13)
	v_pk_mul_f32 v[102:103], v[54:55], v[54:55]
	v_pk_mul_f32 v[104:105], v[52:53], v[52:53]
	v_pk_mul_f32 v[96:97], v[96:97], v[96:97]
	v_pk_mul_f32 v[100:101], v[100:101], v[100:101]
	v_pk_mov_b32 v[108:109], v[104:105], v[102:103] op_sel:[1,0]
	v_mov_b32_e32 v105, v103
	v_pk_fma_f32 v[94:95], v[94:95], v[94:95], v[96:97]
	v_pk_fma_f32 v[96:97], v[98:99], v[98:99], v[100:101]
	s_waitcnt vmcnt(12)
	v_mul_f32_e32 v72, v45, v45
	v_mul_f32_e32 v106, v47, v47
	v_pk_add_f32 v[98:99], v[108:109], v[104:105]
	v_pk_add_f32 v[94:95], v[94:95], v[96:97]
	v_pk_fma_f32 v[102:103], v[44:45], v[44:45], v[72:73] op_sel_hi:[1,1,0]
	v_pk_fma_f32 v[106:107], v[46:47], v[46:47], v[106:107] op_sel_hi:[1,1,0]
	s_waitcnt vmcnt(6)
	v_mul_f32_e32 v81, v48, v48
	v_mul_f32_e32 v110, v49, v49
	v_pk_add_f32 v[98:99], v[98:99], v[98:99] op_sel:[0,1] op_sel_hi:[1,0]
	v_pk_add_f32 v[94:95], v[94:95], v[94:95] op_sel:[0,1] op_sel_hi:[1,0]
	v_pk_mul_f32 v[100:101], v[42:43], v[42:43]
	v_pk_mul_f32 v[104:105], v[40:41], v[40:41]
	v_mul_f32_e32 v103, v50, v50
	v_mul_f32_e32 v107, v51, v51
	v_mov_b32_e32 v99, v110
	v_mov_b32_e32 v95, v81
	v_pk_mov_b32 v[96:97], v[104:105], v[100:101] op_sel:[1,0]
	v_mov_b32_e32 v105, v101
	v_pk_add_f32 v[102:103], v[102:103], v[106:107]
	v_pk_add_f32 v[94:95], v[94:95], v[98:99]
	s_waitcnt vmcnt(4)
; #define GAS __attribute__((address_space(1)))
; __device__ __forceinline__ unsigned pk2(float lo, float hi) { f32x2_m v = {lo, hi}; bf16x2_m b = __builtin_convertvector(v, bf16x2_m); return __builtin_bit_cast(unsigned, b); }
; template <int MODE, bool W8 = false>
; __device__ __forceinline__ void norm_rows(const Ctx& C, const void* src, bf16* xdst, const unsigned char* YS8, const int* srow, const float* gate, const float* gain, bf16* XN, float* outf, unsigned char* XN8 = nullptr) {
;     ...
;             float ss = 0.f;
; #pragma unroll
;             for (int j = 0; j < 8; ++j) ss += (v[q][j].x * v[q][j].x + v[q][j].y * v[q][j].y) + (v[q][j].z * v[q][j].z + v[q][j].w * v[q][j].w);
;             const float rstd = 1.0f / sqrtf(wave_sum(ss) * (1.0f / DM) + RMS_EPS);
;             if (MODE == 1) { GAS v2u* xo = (GAS v2u*)(xdst + (size_t)m * DM) + C.lane;
; #pragma unroll
;                 for (int j = 0; j < 8; ++j) { v2u w; w.x = pk2(v[q][j].x, v[q][j].y); w.y = pk2(v[q][j].z, v[q][j].w); xo[64 * j] = w; } }
;             const GAS f32x4* gg = (const GAS f32x4*)gain + C.lane;
;             if (MODE <= 1) { GAS v2u* o = (GAS v2u*)(XN + (size_t)m * DM) + C.lane;
; #pragma unroll
;                 for (int j = 0; j < 8; ++j) { const f32x4 g = gg[64 * j]; const f32x4 y = v[q][j] * rstd * g; v2u w; w.x = pk2(y.x, y.y); w.y = pk2(y.z, y.w); o[64 * j] = w;
	v_mul_f32_e32 v72, v37, v37
	v_mul_f32_e32 v108, v39, v39
	v_pk_add_f32 v[96:97], v[96:97], v[104:105]
	v_pk_add_f32 v[94:95], v[94:95], v[102:103]
	v_mul_f32_e32 v111, v34, v34
	v_mul_f32_e32 v112, v35, v35
	v_mul_f32_e32 v113, v32, v32
	v_mul_f32_e32 v114, v33, v33
	v_pk_fma_f32 v[100:101], v[36:37], v[36:37], v[72:73] op_sel_hi:[1,1,0]
	v_pk_fma_f32 v[108:109], v[38:39], v[38:39], v[108:109] op_sel_hi:[1,1,0]
	v_pk_add_f32 v[96:97], v[96:97], v[96:97] op_sel:[0,1] op_sel_hi:[1,0]
	v_pk_add_f32 v[94:95], v[94:95], v[94:95] op_sel:[0,1] op_sel_hi:[1,0]
	v_mov_b32_e32 v101, v111
	v_mov_b32_e32 v109, v112
	v_mov_b32_e32 v97, v114
	v_mov_b32_e32 v95, v113
	v_pk_add_f32 v[100:101], v[100:101], v[108:109]
	v_pk_add_f32 v[94:95], v[94:95], v[96:97]
	s_nop 0
	v_pk_add_f32 v[94:95], v[94:95], v[100:101]
	s_nop 0
	v_add_f32_e32 v72, v94, v95
	ds_bpermute_b32 v81, v73, v72
	s_waitcnt lgkmcnt(0)
	v_add_f32_e32 v72, v72, v81
	ds_bpermute_b32 v81, v74, v72
	s_waitcnt lgkmcnt(0)
	v_add_f32_e32 v72, v72, v81
	ds_bpermute_b32 v81, v75, v72
	s_waitcnt lgkmcnt(0)
	v_add_f32_e32 v72, v72, v81
	ds_bpermute_b32 v81, v76, v72
	s_waitcnt lgkmcnt(0)
	v_add_f32_e32 v72, v72, v81
	ds_bpermute_b32 v81, v77, v72
	s_waitcnt lgkmcnt(0)
	v_add_f32_e32 v72, v72, v81
	ds_bpermute_b32 v81, v78, v72
	s_waitcnt lgkmcnt(0)
	v_add_f32_e32 v72, v72, v81
	v_fmamk_f32 v72, v72, 0x3a000000, v79
	v_mul_f32_e32 v81, 0x4f800000, v72
	v_cmp_gt_f32_e32 vcc, s14, v72
	s_nop 1
	v_cndmask_b32_e32 v72, v72, v81, vcc
	v_sqrt_f32_e32 v81, v72
	s_nop 0
	v_add_u32_e32 v94, -1, v81
	v_add_u32_e32 v95, 1, v81
	v_fma_f32 v96, -v94, v81, v72
	v_fma_f32 v97, -v95, v81, v72
	v_cmp_ge_f32_e64 s[2:3], 0, v96
	s_nop 1
	v_cndmask_b32_e64 v81, v81, v94, s[2:3]
	v_cmp_lt_f32_e64 s[2:3], 0, v97
	s_nop 1
	v_cndmask_b32_e64 v81, v81, v95, s[2:3]
	v_mul_f32_e32 v94, 0x37800000, v81
	v_cndmask_b32_e32 v81, v81, v94, vcc
	v_cmp_class_f32_e32 vcc, v72, v80
	s_nop 1
	v_cndmask_b32_e32 v72, v81, v72, vcc
	v_div_scale_f32 v81, s[2:3], v72, v72, 1.0
	v_rcp_f32_e32 v95, v81
	v_div_scale_f32 v94, vcc, 1.0, v72, 1.0
	v_fma_f32 v96, -v81, v95, 1.0
	v_fmac_f32_e32 v95, v96, v95
	v_mul_f32_e32 v96, v94, v95
	v_fma_f32 v97, -v81, v96, v94
	v_fmac_f32_e32 v96, v97, v95
	v_fma_f32 v81, -v81, v96, v94
	v_div_fmas_f32 v81, v81, v95, v96
	v_div_fixup_f32 v72, v81, v72, 1.0
	v_pk_mul_f32 v[86:87], v[86:87], v[72:73] op_sel_hi:[1,0]
	v_pk_mul_f32 v[88:89], v[88:89], v[72:73] op_sel_hi:[1,0]
	v_pk_mul_f32 v[82:83], v[160:161], v[86:87]
	v_pk_mul_f32 v[84:85], v[162:163], v[88:89]
	v_cvt_pk_bf16_f32 v82, v82, v83
	v_cvt_pk_bf16_f32 v83, v84, v85
	global_store_dwordx2 v[70:71], v[82:83], off
	s_nop 1
	v_pk_mul_f32 v[86:87], v[90:91], v[72:73] op_sel_hi:[1,0]
	v_pk_mul_f32 v[88:89], v[92:93], v[72:73] op_sel_hi:[1,0]
	v_pk_mul_f32 v[52:53], v[52:53], v[72:73] op_sel_hi:[1,0]
	v_pk_mul_f32 v[54:55], v[54:55], v[72:73] op_sel_hi:[1,0]
	v_pk_mul_f32 v[44:45], v[44:45], v[72:73] op_sel_hi:[1,0]
	v_pk_mul_f32 v[46:47], v[46:47], v[72:73] op_sel_hi:[1,0]
	v_pk_mul_f32 v[48:49], v[48:49], v[72:73] op_sel_hi:[1,0]
	v_pk_mul_f32 v[50:51], v[50:51], v[72:73] op_sel_hi:[1,0]
	v_pk_mul_f32 v[40:41], v[40:41], v[72:73] op_sel_hi:[1,0]
	v_pk_mul_f32 v[42:43], v[42:43], v[72:73] op_sel_hi:[1,0]
	v_pk_mul_f32 v[36:37], v[36:37], v[72:73] op_sel_hi:[1,0]
	v_pk_mul_f32 v[38:39], v[38:39], v[72:73] op_sel_hi:[1,0]
	v_pk_mul_f32 v[32:33], v[32:33], v[72:73] op_sel_hi:[1,0]
	v_pk_mul_f32 v[34:35], v[34:35], v[72:73] op_sel_hi:[1,0]
	s_waitcnt vmcnt(4)
	v_mul_f32_e32 v81, v24, v24
	s_waitcnt vmcnt(1)
	v_pk_mul_f32 v[84:85], v[166:167], v[88:89]
	v_pk_mul_f32 v[82:83], v[164:165], v[86:87]
	v_mul_f32_e32 v86, v16, v16
	v_cvt_pk_bf16_f32 v82, v82, v83
	v_cvt_pk_bf16_f32 v83, v84, v85
	global_store_dwordx2 v[70:71], v[82:83], off offset:512
	s_nop 1
	v_mul_f32_e32 v87, v17, v17
	v_mul_f32_e32 v88, v18, v18
	v_mul_f32_e32 v89, v19, v19
	v_pk_mul_f32 v[54:55], v[170:171], v[54:55]
	v_pk_mul_f32 v[52:53], v[168:169], v[52:53]
	v_pk_mul_f32 v[82:83], v[4:5], v[4:5]
	v_cvt_pk_bf16_f32 v52, v52, v53
	v_cvt_pk_bf16_f32 v53, v54, v55
	global_store_dwordx2 v[70:71], v[52:53], off offset:1024
	s_nop 1
	v_mul_f32_e32 v84, v1, v1
	v_pk_mul_f32 v[46:47], v[174:175], v[46:47]
	v_pk_mul_f32 v[44:45], v[172:173], v[44:45]
	v_mov_b32_e32 v52, v15
	v_cvt_pk_bf16_f32 v44, v44, v45
	v_cvt_pk_bf16_f32 v45, v46, v47
	global_store_dwordx2 v[70:71], v[44:45], off offset:1536
	s_nop 1
	v_mov_b32_e32 v53, v11
	v_pk_mul_f32 v[54:55], v[6:7], v[6:7]
	v_pk_mul_f32 v[46:47], v[178:179], v[50:51]
	v_pk_mul_f32 v[44:45], v[176:177], v[48:49]
	v_mov_b32_e32 v48, v13
	v_cvt_pk_bf16_f32 v44, v44, v45
	v_cvt_pk_bf16_f32 v45, v46, v47
	global_store_dwordx2 v[70:71], v[44:45], off offset:2048
	s_nop 1
	v_mov_b32_e32 v49, v9
	v_mov_b32_e32 v50, v14
	v_mov_b32_e32 v51, v10
	v_pk_mul_f32 v[42:43], v[42:43], v[182:183]
	v_pk_mul_f32 v[40:41], v[40:41], v[180:181]
	v_mov_b32_e32 v46, v12
	v_cvt_pk_bf16_f32 v40, v40, v41
	v_cvt_pk_bf16_f32 v41, v42, v43
	global_store_dwordx2 v[70:71], v[40:41], off offset:2560
	s_nop 1
	v_mov_b32_e32 v47, v8
	v_lshl_add_u64 v[44:45], s[4:5], 0, v[68:69]
	v_add_co_u32_e32 v44, vcc, s15, v44
	s_add_u32 s4, s4, 0x1000000
	s_nop 0
	v_addc_co_u32_e32 v45, vcc, 0, v45, vcc
	s_addc_u32 s5, s5, 0
	s_add_u32 s6, s6, 0x2000000
	s_addc_u32 s7, s7, 0
	s_add_u32 s8, s8, 0x2000000
	s_addc_u32 s9, s9, 0
	s_add_u32 s10, s10, 0x1000000
	s_addc_u32 s11, s11, 0
	s_cmpk_lt_i32 s12, 0x3000
	v_pk_mul_f32 v[38:39], v[38:39], v[186:187]
	v_pk_mul_f32 v[36:37], v[36:37], v[184:185]
	v_pk_mul_f32 v[42:43], v[48:49], v[48:49]
	v_cvt_pk_bf16_f32 v36, v36, v37
	v_cvt_pk_bf16_f32 v37, v38, v39
; #define GAS __attribute__((address_space(1)))
; __device__ __forceinline__ unsigned pk2(float lo, float hi) { f32x2_m v = {lo, hi}; bf16x2_m b = __builtin_convertvector(v, bf16x2_m); return __builtin_bit_cast(unsigned, b); }
; template <int MODE, bool W8 = false>
; __device__ __forceinline__ void norm_rows(const Ctx& C, const void* src, bf16* xdst, const unsigned char* YS8, const int* srow, const float* gate, const float* gain, bf16* XN, float* outf, unsigned char* XN8 = nullptr) {
;     ...
;             float ss = 0.f;
; #pragma unroll
;             for (int j = 0; j < 8; ++j) ss += (v[q][j].x * v[q][j].x + v[q][j].y * v[q][j].y) + (v[q][j].z * v[q][j].z + v[q][j].w * v[q][j].w);
;             const float rstd = 1.0f / sqrtf(wave_sum(ss) * (1.0f / DM) + RMS_EPS);
;             if (MODE == 1) { GAS v2u* xo = (GAS v2u*)(xdst + (size_t)m * DM) + C.lane;
; #pragma unroll
;                 for (int j = 0; j < 8; ++j) { v2u w; w.x = pk2(v[q][j].x, v[q][j].y); w.y = pk2(v[q][j].z, v[q][j].w); xo[64 * j] = w; } }
;             const GAS f32x4* gg = (const GAS f32x4*)gain + C.lane;
;             if (MODE <= 1) { GAS v2u* o = (GAS v2u*)(XN + (size_t)m * DM) + C.lane;
; #pragma unroll
;                 for (int j = 0; j < 8; ++j) { const f32x4 g = gg[64 * j]; const f32x4 y = v[q][j] * rstd * g; v2u w; w.x = pk2(y.x, y.y); w.y = pk2(y.z, y.w); o[64 * j] = w;
	global_store_dwordx2 v[70:71], v[36:37], off offset:3072
	s_nop 1
	v_pk_mul_f32 v[48:49], v[52:53], v[52:53]
	v_mul_f32_e32 v40, v3, v3
	v_pk_mov_b32 v[52:53], v[82:83], v[54:55] op_sel:[1,0]
	v_mov_b32_e32 v83, v55
	v_pk_fma_f32 v[42:43], v[46:47], v[46:47], v[42:43]
	v_pk_fma_f32 v[46:47], v[50:51], v[50:51], v[48:49]
	v_pk_fma_f32 v[40:41], v[2:3], v[2:3], v[40:41] op_sel_hi:[1,1,0]
	v_pk_add_f32 v[48:49], v[52:53], v[82:83]
	v_pk_add_f32 v[42:43], v[42:43], v[46:47]
	v_pk_fma_f32 v[54:55], v[0:1], v[0:1], v[84:85] op_sel_hi:[1,1,0]
	v_mul_f32_e32 v41, v25, v25
	v_mul_f32_e32 v83, v27, v27
	v_pk_add_f32 v[46:47], v[48:49], v[48:49] op_sel:[0,1] op_sel_hi:[1,0]
	v_pk_add_f32 v[42:43], v[42:43], v[42:43] op_sel:[0,1] op_sel_hi:[1,0]
	v_mul_f32_e32 v55, v26, v26
	v_pk_mul_f32 v[48:49], v[22:23], v[22:23]
	v_pk_mul_f32 v[50:51], v[20:21], v[20:21]
	v_mov_b32_e32 v47, v41
	v_mov_b32_e32 v41, v83
	v_mov_b32_e32 v43, v81
	v_pk_mov_b32 v[84:85], v[50:51], v[48:49] op_sel:[1,0]
	v_mov_b32_e32 v51, v49
	v_pk_add_f32 v[40:41], v[54:55], v[40:41]
	v_pk_add_f32 v[42:43], v[42:43], v[46:47]
	v_mul_f32_e32 v52, v29, v29
	v_mul_f32_e32 v82, v31, v31
	v_pk_add_f32 v[50:51], v[84:85], v[50:51]
	v_pk_add_f32 v[40:41], v[42:43], v[40:41]
	v_pk_fma_f32 v[48:49], v[28:29], v[28:29], v[52:53] op_sel_hi:[1,1,0]
	v_pk_fma_f32 v[52:53], v[30:31], v[30:31], v[82:83] op_sel_hi:[1,1,0]
	v_pk_add_f32 v[46:47], v[50:51], v[50:51] op_sel:[0,1] op_sel_hi:[1,0]
	v_pk_add_f32 v[40:41], v[40:41], v[40:41] op_sel:[0,1] op_sel_hi:[1,0]
	v_mov_b32_e32 v49, v88
	v_mov_b32_e32 v53, v89
	v_mov_b32_e32 v47, v87
	v_mov_b32_e32 v41, v86
	v_pk_add_f32 v[48:49], v[48:49], v[52:53]
	v_pk_add_f32 v[40:41], v[40:41], v[46:47]
	v_pk_mul_f32 v[34:35], v[34:35], v[190:191]
	v_pk_mul_f32 v[32:33], v[32:33], v[188:189]
	v_pk_add_f32 v[40:41], v[40:41], v[48:49]
	v_cvt_pk_bf16_f32 v32, v32, v33
	v_cvt_pk_bf16_f32 v33, v34, v35
	global_store_dwordx2 v[70:71], v[32:33], off offset:3584
	s_nop 1
	v_add_f32_e32 v40, v40, v41
	ds_bpermute_b32 v41, v73, v40
	s_waitcnt lgkmcnt(0)
	v_add_f32_e32 v40, v40, v41
	ds_bpermute_b32 v41, v74, v40
	s_waitcnt lgkmcnt(0)
	v_add_f32_e32 v40, v40, v41
	ds_bpermute_b32 v36, v75, v40
	s_waitcnt lgkmcnt(0)
	v_add_f32_e32 v36, v40, v36
	ds_bpermute_b32 v37, v76, v36
	s_waitcnt lgkmcnt(0)
	v_add_f32_e32 v36, v36, v37
	ds_bpermute_b32 v37, v77, v36
	s_waitcnt lgkmcnt(0)
	v_add_f32_e32 v36, v36, v37
	ds_bpermute_b32 v37, v78, v36
	s_waitcnt lgkmcnt(0)
	v_add_f32_e32 v36, v36, v37
	v_fmamk_f32 v36, v36, 0x3a000000, v79
	v_mul_f32_e32 v37, 0x4f800000, v36
	v_cmp_gt_f32_e32 vcc, s14, v36
	s_nop 1
	v_cndmask_b32_e32 v36, v36, v37, vcc
	v_sqrt_f32_e32 v37, v36
	s_nop 0
	v_add_u32_e32 v38, -1, v37
	v_add_u32_e32 v39, 1, v37
	v_fma_f32 v40, -v38, v37, v36
	v_fma_f32 v41, -v39, v37, v36
	v_cmp_ge_f32_e64 s[2:3], 0, v40
	s_nop 1
	v_cndmask_b32_e64 v37, v37, v38, s[2:3]
	v_cmp_lt_f32_e64 s[2:3], 0, v41
	s_nop 1
	v_cndmask_b32_e64 v37, v37, v39, s[2:3]
	v_mul_f32_e32 v38, 0x37800000, v37
	v_cndmask_b32_e32 v37, v37, v38, vcc
	v_cmp_class_f32_e32 vcc, v36, v80
	s_nop 1
	v_cndmask_b32_e32 v36, v37, v36, vcc
	v_div_scale_f32 v37, s[2:3], v36, v36, 1.0
	v_rcp_f32_e32 v39, v37
	v_div_scale_f32 v38, vcc, 1.0, v36, 1.0
	v_fma_f32 v40, -v37, v39, 1.0
	v_fmac_f32_e32 v39, v40, v39
	v_mul_f32_e32 v40, v38, v39
	v_fma_f32 v41, -v37, v40, v38
	v_fmac_f32_e32 v40, v41, v39
	v_fma_f32 v37, -v37, v40, v38
	v_div_fmas_f32 v37, v37, v39, v40
	v_div_fixup_f32 v36, v37, v36, 1.0
	v_pk_mul_f32 v[12:13], v[12:13], v[36:37] op_sel_hi:[1,0]
	v_pk_mul_f32 v[14:15], v[14:15], v[36:37] op_sel_hi:[1,0]
	v_pk_mul_f32 v[12:13], v[160:161], v[12:13]
	v_pk_mul_f32 v[14:15], v[162:163], v[14:15]
	v_cvt_pk_bf16_f32 v12, v12, v13
	v_cvt_pk_bf16_f32 v13, v14, v15
	global_store_dwordx2 v[44:45], v[12:13], off
	s_nop 1
	v_pk_mul_f32 v[8:9], v[8:9], v[36:37] op_sel_hi:[1,0]
	v_pk_mul_f32 v[10:11], v[10:11], v[36:37] op_sel_hi:[1,0]
	v_pk_mul_f32 v[4:5], v[4:5], v[36:37] op_sel_hi:[1,0]
	v_pk_mul_f32 v[6:7], v[6:7], v[36:37] op_sel_hi:[1,0]
	v_pk_mul_f32 v[0:1], v[0:1], v[36:37] op_sel_hi:[1,0]
	v_pk_mul_f32 v[2:3], v[2:3], v[36:37] op_sel_hi:[1,0]
	v_pk_mul_f32 v[10:11], v[166:167], v[10:11]
	v_pk_mul_f32 v[8:9], v[164:165], v[8:9]
	s_nop 0
	v_cvt_pk_bf16_f32 v8, v8, v9
	v_cvt_pk_bf16_f32 v9, v10, v11
	global_store_dwordx2 v[44:45], v[8:9], off offset:512
	s_nop 1
	v_pk_mul_f32 v[6:7], v[170:171], v[6:7]
	v_pk_mul_f32 v[4:5], v[168:169], v[4:5]
	s_nop 0
	v_cvt_pk_bf16_f32 v4, v4, v5
	v_cvt_pk_bf16_f32 v5, v6, v7
	global_store_dwordx2 v[44:45], v[4:5], off offset:1024
	s_nop 1
	v_pk_mul_f32 v[2:3], v[174:175], v[2:3]
	v_pk_mul_f32 v[0:1], v[172:173], v[0:1]
	v_pk_mul_f32 v[4:5], v[24:25], v[36:37] op_sel_hi:[1,0]
	v_cvt_pk_bf16_f32 v0, v0, v1
	v_cvt_pk_bf16_f32 v1, v2, v3
	global_store_dwordx2 v[44:45], v[0:1], off offset:1536
	s_nop 1
	v_pk_mul_f32 v[6:7], v[26:27], v[36:37] op_sel_hi:[1,0]
	v_pk_mul_f32 v[0:1], v[176:177], v[4:5]
	v_pk_mul_f32 v[2:3], v[178:179], v[6:7]
	v_cvt_pk_bf16_f32 v0, v0, v1
	v_cvt_pk_bf16_f32 v1, v2, v3
	global_store_dwordx2 v[44:45], v[0:1], off offset:2048
	s_nop 1
	v_pk_mul_f32 v[4:5], v[20:21], v[36:37] op_sel_hi:[1,0]
	v_pk_mul_f32 v[6:7], v[22:23], v[36:37] op_sel_hi:[1,0]
	v_pk_mul_f32 v[0:1], v[4:5], v[180:181]
	v_pk_mul_f32 v[2:3], v[6:7], v[182:183]
	v_cvt_pk_bf16_f32 v0, v0, v1
	v_cvt_pk_bf16_f32 v1, v2, v3
	global_store_dwordx2 v[44:45], v[0:1], off offset:2560
	s_nop 1
	v_pk_mul_f32 v[4:5], v[28:29], v[36:37] op_sel_hi:[1,0]
	v_pk_mul_f32 v[6:7], v[30:31], v[36:37] op_sel_hi:[1,0]
	v_pk_mul_f32 v[0:1], v[4:5], v[184:185]
	v_pk_mul_f32 v[2:3], v[6:7], v[186:187]
	v_cvt_pk_bf16_f32 v0, v0, v1
	v_cvt_pk_bf16_f32 v1, v2, v3
	global_store_dwordx2 v[44:45], v[0:1], off offset:3072
	s_nop 1
	v_pk_mul_f32 v[4:5], v[16:17], v[36:37] op_sel_hi:[1,0]
	v_pk_mul_f32 v[6:7], v[18:19], v[36:37] op_sel_hi:[1,0]
	v_pk_mul_f32 v[0:1], v[4:5], v[188:189]
	v_pk_mul_f32 v[2:3], v[6:7], v[190:191]
	v_cvt_pk_bf16_f32 v0, v0, v1
	v_cvt_pk_bf16_f32 v1, v2, v3
	global_store_dwordx2 v[44:45], v[0:1], off offset:3584
	s_nop 1
	s_cbranch_scc1 .LBB0_122

; #define GAS __attribute__((address_space(1)))
; __device__ __forceinline__ float bflo(unsigned w) { return __uint_as_float(w << 16); }
; __device__ __forceinline__ float bfhi(unsigned w) { return __uint_as_float(w & 0xffff0000u); }
; template <int MODE, bool W8 = false>
; __device__ __forceinline__ void norm_rows(const Ctx& C, const void* src, bf16* xdst, const unsigned char* YS8, const int* srow, const float* gate, const float* gain, bf16* XN, float* outf, unsigned char* XN8 = nullptr) {
;     ...
;     for (int m0 = C.gw; m0 < T; m0 += NR * C.NGW) {
;         f32x4 v[NR][8]; unsigned ya[NR][8], yb[NR][8]; float h0[NR], h1[NR];
; #pragma unroll
;         for (int q = 0; q < NR; ++q) { const int m = m0 + q * C.NGW;
;             if (MODE == 0) { const GAS f32x4* xr = (const GAS f32x4*)((const float*)src + (size_t)m * DM) + C.lane;
; #pragma unroll
;                 for (int j = 0; j < 8; ++j) v[q][j] = xr[64 * j]; }
;             else { const GAS v2u* xr = (const GAS v2u*)((const bf16*)src + (size_t)m * DM) + C.lane;
; #pragma unroll
;                 for (int j = 0; j < 8; ++j) { const v2u t_ = xr[64 * j]; v[q][j] = (f32x4){bflo(t_.x), bfhi(t_.x), bflo(t_.y), bfhi(t_.y)}; } }
;             if (MODE >= 1) {
;                 h0[q] = gate[2 * m] * (1.0f / SY); h1[q] = gate[2 * m + 1] * (1.0f / SY);
;                 const GAS unsigned* y0 = (const GAS unsigned*)(YS8 + (size_t)srow[2 * m] * DM) + C.lane; const GAS unsigned* y1 = (const GAS unsigned*)(YS8 + (size_t)srow[2 * m + 1] * DM) + C.lane;
; #pragma unroll
;                 for (int j = 0; j < 8; ++j) { ya[q][j] = y0[64 * j]; yb[q][j] = y1[64 * j]; } } }
;     ...
;             const GAS f32x4* gg = (const GAS f32x4*)gain + C.lane;
.LBB0_1318:
	v_readlane_b32 s0, v253, 16
	s_waitcnt vmcnt(0)
	v_mbcnt_lo_u32_b32 v16, -1, 0
	v_mbcnt_hi_u32_b32 v16, -1, v16
	v_readlane_b32 s1, v253, 18
	v_readlane_b32 s16, v253, 8
	v_add_u32_e32 v0, s0, v16
	v_readlane_b32 s0, v253, 19
	s_mov_b32 s6, s1
	v_readlane_b32 s1, v253, 17
	v_add_u32_e32 v1, s0, v0
	v_readlane_b32 s0, v253, 0
	v_readlane_b32 s18, v253, 10
	v_readlane_b32 s19, v253, 11
	s_mov_b64 s[4:5], s[18:19]
	s_add_u32 s0, s4, 0x62800000
	v_readlane_b32 s22, v253, 14
	s_addc_u32 s1, s5, 0
	v_readlane_b32 s23, v253, 15
	s_add_u32 s22, s4, 0x6a820000
	s_addc_u32 s23, s5, 0
	s_add_u32 s24, s4, 0x6a840000
	s_addc_u32 s25, s5, 0
	s_cmpk_lt_i32 s6, 0x4000
	s_cselect_b64 s[10:11], -1, 0
	v_readlane_b32 s8, v253, 1
	v_cndmask_b32_e64 v0, 0, 1, s[10:11]
	v_readlane_b32 s9, v253, 2
	s_mov_b64 s[2:3], -1
	s_and_b64 vcc, exec, s[14:15]
	v_cmp_ne_u32_e64 s[36:37], 1, v0
	v_readlane_b32 s17, v253, 9
	v_readlane_b32 s20, v253, 12
	v_readlane_b32 s21, v253, 13
	s_cbranch_vccz .LBB0_1323
	s_and_b64 vcc, exec, s[36:37]
	s_movk_i32 s27, 0x1000
	s_mov_b32 s30, 0xf800000
	s_mov_b32 s34, 0x4b800000
	s_cbranch_vccnz .LBB0_1322
	v_and_b32_e32 v0, 64, v215
	v_add_u32_e32 v0, 64, v0
	v_xor_b32_e32 v1, 1, v215
	v_cmp_lt_i32_e32 vcc, v1, v0
	s_load_dwordx2 s[2:3], s[8:9], 0xc8
	v_ashrrev_i32_e32 v17, 31, v16
	v_cndmask_b32_e32 v1, v215, v1, vcc
	v_lshlrev_b32_e32 v3, 2, v1
	v_xor_b32_e32 v1, 2, v215
	v_cmp_lt_i32_e32 vcc, v1, v0
	s_add_i32 s26, s6, 0xfffff000
	s_lshl_b32 s10, s6, 1
	v_cndmask_b32_e32 v1, v215, v1, vcc
	v_lshlrev_b32_e32 v27, 2, v1
	v_xor_b32_e32 v1, 4, v215
	v_cmp_lt_i32_e32 vcc, v1, v0
	v_readlane_b32 s40, v253, 8
	v_readlane_b32 s41, v253, 9
	v_cndmask_b32_e32 v1, v215, v1, vcc
	v_lshlrev_b32_e32 v77, 2, v1
	v_xor_b32_e32 v1, 8, v215
	v_cmp_lt_i32_e32 vcc, v1, v0
	v_lshl_add_u64 v[20:21], v[16:17], 2, s[0:1]
	v_lshlrev_b64 v[22:23], 3, v[16:17]
	v_cndmask_b32_e32 v1, v215, v1, vcc
	v_lshlrev_b32_e32 v80, 2, v1
	v_xor_b32_e32 v1, 16, v215
	v_cmp_lt_i32_e32 vcc, v1, v0
	v_readlane_b32 s42, v253, 10
	v_readlane_b32 s43, v253, 11
	v_cndmask_b32_e32 v1, v215, v1, vcc
	v_lshlrev_b32_e32 v81, 2, v1
	v_xor_b32_e32 v1, 32, v215
	v_cmp_lt_i32_e32 vcc, v1, v0
	v_readlane_b32 s44, v253, 12
	v_readlane_b32 s45, v253, 13
	v_cndmask_b32_e32 v0, v215, v1, vcc
	v_lshlrev_b32_e32 v82, 2, v0
	v_lshlrev_b64 v[0:1], 4, v[16:17]
	s_waitcnt lgkmcnt(0)
	v_lshl_add_u64 v[8:9], s[2:3], 0, v[0:1]
	s_mov_b64 s[2:3], 0x1000
	v_lshl_add_u64 v[10:11], v[8:9], 0, s[2:3]
	s_mov_b64 s[2:3], 0x1400
	v_lshl_add_u64 v[12:13], v[8:9], 0, s[2:3]
	s_mov_b64 s[2:3], 0x1800
	v_lshl_add_u64 v[14:15], v[8:9], 0, s[2:3]
	s_mov_b64 s[2:3], 0x1c00
	v_lshl_add_u64 v[18:19], v[8:9], 0, s[2:3]
	s_add_i32 s2, s6, 0x800
	s_ashr_i32 s3, s2, 31
	s_lshl_b64 s[12:13], s[2:3], 13
	s_add_u32 s12, s40, s12
	s_addc_u32 s13, s41, s13
	s_ashr_i32 s7, s6, 31
	s_lshl_b64 s[16:17], s[6:7], 12
	s_add_u32 s16, s4, s16
	s_addc_u32 s17, s5, s17
	s_lshl_b64 s[2:3], s[2:3], 12
	s_add_u32 s18, s4, s2
	s_addc_u32 s19, s5, s3
	s_lshl_b64 s[2:3], s[6:7], 13
	s_add_u32 s20, s40, s2
	s_addc_u32 s21, s41, s3
	v_readlane_b32 s46, v253, 14
	v_readlane_b32 s47, v253, 15
	global_load_dwordx4 v[160:163], v[8:9], off
	global_load_dwordx4 v[164:167], v[8:9], off offset:1024
	global_load_dwordx4 v[168:171], v[8:9], off offset:2048
	global_load_dwordx4 v[172:175], v[8:9], off offset:3072
	global_load_dwordx4 v[176:179], v[10:11], off
	global_load_dwordx4 v[180:183], v[12:13], off
	global_load_dwordx4 v[184:187], v[14:15], off
	global_load_dwordx4 v[188:191], v[18:19], off
.LBB0_1321:
	s_ashr_i32 s11, s10, 31
	s_lshl_b64 s[2:3], s[10:11], 2
	s_add_u32 s28, s24, s2
	s_addc_u32 s29, s25, s3
	global_load_dwordx2 v[192:193], v2, s[28:29]
	s_add_u32 s2, s22, s2
	s_addc_u32 s3, s23, s3
	global_load_dwordx2 v[194:195], v2, s[2:3]
	s_ashr_i32 s11, s10, 31
	v_lshl_add_u64 v[4:5], s[16:17], 0, v[22:23]
	s_lshl_b64 s[2:3], s[10:11], 2
	v_add_co_u32_e32 v4, vcc, 0x4b800000, v4
	s_add_u32 s28, s24, s2
	s_nop 0
	v_addc_co_u32_e32 v5, vcc, 0, v5, vcc
	s_addc_u32 s29, s25, s3
	global_load_dwordx2 v[58:59], v[4:5], off
	global_load_dwordx2 v[52:53], v[4:5], off offset:512
	global_load_dwordx2 v[50:51], v[4:5], off offset:1024
	global_load_dwordx2 v[48:49], v[4:5], off offset:1536
	global_load_dwordx2 v[44:45], v[4:5], off offset:2048
	global_load_dwordx2 v[46:47], v[4:5], off offset:2560
	global_load_dwordx2 v[6:7], v[4:5], off offset:3072
	s_nop 0
	global_load_dwordx2 v[4:5], v[4:5], off offset:3584
	s_waitcnt vmcnt(7)
	v_lshlrev_b32_e32 v66, 16, v58
	s_add_i32 s28, s10, 1
	s_ashr_i32 s29, s28, 31
	s_add_u32 s2, s22, s2
	s_addc_u32 s3, s23, s3
	v_and_b32_e32 v67, 0xffff0000, v58
	v_lshlrev_b32_e32 v58, 16, v59
	v_and_b32_e32 v59, 0xffff0000, v59
	s_waitcnt vmcnt(1)
	v_and_b32_e32 v99, 0xffff0000, v6
	s_waitcnt vmcnt(0)
	v_mul_f32_e32 v54, 0x3d800000, v192
	v_mov_b32_e32 v24, v194
	s_lshl_b64 s[2:3], s[28:29], 2
	s_add_u32 s2, s22, s2
	s_addc_u32 s3, s23, s3
	v_mov_b32_e32 v28, v195
	v_mul_f32_e32 v76, 0x3d800000, v193
	s_add_i32 s2, s10, 0x1000
	s_ashr_i32 s3, s2, 31
	s_lshl_b64 s[2:3], s[2:3], 2
	s_add_u32 s28, s24, s2
	s_addc_u32 s29, s25, s3
	s_waitcnt vmcnt(1)
	v_ashrrev_i32_e32 v25, 31, v24
	v_lshlrev_b64 v[24:25], 11, v[24:25]
	v_lshl_add_u64 v[24:25], v[20:21], 0, v[24:25]
	s_waitcnt vmcnt(0)
; #define GAS __attribute__((address_space(1)))
; __device__ __forceinline__ float bflo(unsigned w) { return __uint_as_float(w << 16); }
; __device__ __forceinline__ float bfhi(unsigned w) { return __uint_as_float(w & 0xffff0000u); }
; template <int MODE, bool W8 = false>
; __device__ __forceinline__ void norm_rows(const Ctx& C, const void* src, bf16* xdst, const unsigned char* YS8, const int* srow, const float* gate, const float* gain, bf16* XN, float* outf, unsigned char* XN8 = nullptr) {
;     ...
;         for (int q = 0; q < NR; ++q) { const int m = m0 + q * C.NGW;
;             if (MODE == 0) { const GAS f32x4* xr = (const GAS f32x4*)((const float*)src + (size_t)m * DM) + C.lane;
; #pragma unroll
;                 for (int j = 0; j < 8; ++j) v[q][j] = xr[64 * j]; }
;             else { const GAS v2u* xr = (const GAS v2u*)((const bf16*)src + (size_t)m * DM) + C.lane;
; #pragma unroll
;                 for (int j = 0; j < 8; ++j) { const v2u t_ = xr[64 * j]; v[q][j] = (f32x4){bflo(t_.x), bfhi(t_.x), bflo(t_.y), bfhi(t_.y)}; } }
;             if (MODE >= 1) {
;                 h0[q] = gate[2 * m] * (1.0f / SY); h1[q] = gate[2 * m + 1] * (1.0f / SY);
;                 const GAS unsigned* y0 = (const GAS unsigned*)(YS8 + (size_t)srow[2 * m] * DM) + C.lane; const GAS unsigned* y1 = (const GAS unsigned*)(YS8 + (size_t)srow[2 * m + 1] * DM) + C.lane;
; #pragma unroll
;                 for (int j = 0; j < 8; ++j) { ya[q][j] = y0[64 * j]; yb[q][j] = y1[64 * j]; } } }
; #pragma unroll
;         for (int q = 0; q < NR; ++q) { const int m = m0 + q * C.NGW;
;             if (MODE >= 1) {
; #pragma unroll
;                 for (int j = 0; j < 8; ++j) { const unsigned a = ya[q][j], b = yb[q][j];
;                     const f32x2_m a01 = __builtin_amdgcn_cvt_pk_f32_fp8((int)a, false), a23 = __builtin_amdgcn_cvt_pk_f32_fp8((int)a, true), b01 = __builtin_amdgcn_cvt_pk_f32_fp8((int)b, false), b23 = __builtin_amdgcn_cvt_pk_f32_fp8((int)b, true);
;                     v[q][j].x += h0[q] * a01.x + h1[q] * b01.x; v[q][j].y += h0[q] * a01.y + h1[q] * b01.y; v[q][j].z += h0[q] * a23.x + h1[q] * b23.x; v[q][j].w += h0[q] * a23.y + h1[q] * b23.y; } }
	v_ashrrev_i32_e32 v29, 31, v28
	v_lshlrev_b64 v[28:29], 11, v[28:29]
	v_lshl_add_u64 v[28:29], v[20:21], 0, v[28:29]
	global_load_dword v55, v[24:25], off
	global_load_dword v64, v[28:29], off
	global_load_dword v68, v[24:25], off offset:256
	global_load_dword v69, v[28:29], off offset:256
	global_load_dword v70, v[24:25], off offset:512
	global_load_dword v71, v[28:29], off offset:512
	global_load_dword v72, v[24:25], off offset:768
	global_load_dword v73, v[28:29], off offset:768
	global_load_dword v74, v[24:25], off offset:1024
	global_load_dword v75, v[28:29], off offset:1024
	global_load_dword v78, v[24:25], off offset:1280
	global_load_dword v79, v[28:29], off offset:1280
	global_load_dword v97, v[24:25], off offset:1536
	global_load_dword v98, v[28:29], off offset:1536
	global_load_dword v100, v[24:25], off offset:1792
	global_load_dword v101, v[28:29], off offset:1792
	v_lshl_add_u64 v[24:25], s[18:19], 0, v[22:23]
	v_add_co_u32_e32 v24, vcc, s34, v24
	s_waitcnt vmcnt(14)
	v_cvt_pk_f32_fp8_e32 v[62:63], v64
	v_addc_co_u32_e32 v25, vcc, 0, v25, vcc
	global_load_dwordx2 v[42:43], v[24:25], off
	global_load_dwordx2 v[40:41], v[24:25], off offset:512
	global_load_dwordx2 v[38:39], v[24:25], off offset:1024
	global_load_dwordx2 v[36:37], v[24:25], off offset:1536
	global_load_dwordx2 v[34:35], v[24:25], off offset:2048
	global_load_dwordx2 v[32:33], v[24:25], off offset:2560
	global_load_dwordx2 v[30:31], v[24:25], off offset:3072
	s_nop 0
	global_load_dwordx2 v[24:25], v[24:25], off offset:3584
	v_cvt_pk_f32_fp8_sdwa v[64:65], v64 src0_sel:WORD_1
	global_load_dwordx2 v[28:29], v2, s[28:29]
	s_add_i32 s28, s10, 0x1001
	s_ashr_i32 s29, s28, 31
	s_add_u32 s2, s22, s2
	s_addc_u32 s3, s23, s3
	global_load_dword v56, v2, s[2:3]
	s_lshl_b64 s[2:3], s[28:29], 2
	s_add_u32 s2, s22, s2
	s_addc_u32 s3, s23, s3
	global_load_dword v60, v2, s[2:3]
	v_pk_mul_f32 v[62:63], v[76:77], v[62:63] op_sel_hi:[0,1]
	s_addk_i32 s26, 0x1000
	s_addk_i32 s10, 0x2000
	s_waitcnt vmcnt(2)
	v_mul_f32_e32 v26, 0x3d800000, v28
	v_mul_f32_e32 v28, 0x3d800000, v29
	s_waitcnt vmcnt(1)
	v_ashrrev_i32_e32 v57, 31, v56
	v_lshlrev_b64 v[56:57], 11, v[56:57]
	v_lshl_add_u64 v[56:57], v[20:21], 0, v[56:57]
	s_waitcnt vmcnt(0)
	v_ashrrev_i32_e32 v61, 31, v60
	v_lshlrev_b64 v[60:61], 11, v[60:61]
	v_lshl_add_u64 v[60:61], v[20:21], 0, v[60:61]
	global_load_dword v96, v[56:57], off
	global_load_dword v95, v[60:61], off
	global_load_dword v94, v[56:57], off offset:256
	global_load_dword v93, v[60:61], off offset:256
	global_load_dword v92, v[56:57], off offset:512
	global_load_dword v91, v[60:61], off offset:512
	global_load_dword v90, v[56:57], off offset:768
	global_load_dword v89, v[60:61], off offset:768
	global_load_dword v88, v[56:57], off offset:1024
	global_load_dword v87, v[60:61], off offset:1024
	global_load_dword v86, v[56:57], off offset:1280
	global_load_dword v85, v[60:61], off offset:1280
	global_load_dword v84, v[56:57], off offset:1536
	global_load_dword v83, v[60:61], off offset:1536
	global_load_dword v29, v[56:57], off offset:1792
	global_load_dword v17, v[60:61], off offset:1792
	v_cvt_pk_f32_fp8_e32 v[56:57], v55
	v_cvt_pk_f32_fp8_sdwa v[60:61], v55 src0_sel:WORD_1
	v_pk_fma_f32 v[56:57], v[54:55], v[56:57], v[62:63] op_sel_hi:[0,1,1]
	v_pk_mul_f32 v[62:63], v[76:77], v[64:65] op_sel_hi:[0,1]
	v_pk_fma_f32 v[60:61], v[54:55], v[60:61], v[62:63] op_sel_hi:[0,1,1]
	v_cvt_pk_f32_fp8_e32 v[64:65], v69
	v_pk_add_f32 v[56:57], v[56:57], v[66:67]
	v_pk_add_f32 v[62:63], v[60:61], v[58:59]
	v_cvt_pk_f32_fp8_e32 v[58:59], v68
	v_cvt_pk_f32_fp8_sdwa v[66:67], v69 src0_sel:WORD_1
	v_cvt_pk_f32_fp8_sdwa v[60:61], v68 src0_sel:WORD_1
	v_pk_mul_f32 v[64:65], v[76:77], v[64:65] op_sel_hi:[0,1]
	v_pk_fma_f32 v[58:59], v[54:55], v[58:59], v[64:65] op_sel_hi:[0,1,1]
	v_pk_mul_f32 v[64:65], v[76:77], v[66:67] op_sel_hi:[0,1]
	v_lshlrev_b32_e32 v68, 16, v52
	v_and_b32_e32 v69, 0xffff0000, v52
	v_lshlrev_b32_e32 v52, 16, v53
	v_and_b32_e32 v53, 0xffff0000, v53
	v_pk_fma_f32 v[60:61], v[54:55], v[60:61], v[64:65] op_sel_hi:[0,1,1]
	v_pk_add_f32 v[66:67], v[60:61], v[52:53]
	v_cvt_pk_f32_fp8_e32 v[60:61], v71
	v_cvt_pk_f32_fp8_e32 v[52:53], v70
	v_pk_add_f32 v[58:59], v[58:59], v[68:69]
	v_cvt_pk_f32_fp8_sdwa v[68:69], v71 src0_sel:WORD_1
	v_cvt_pk_f32_fp8_sdwa v[64:65], v70 src0_sel:WORD_1
	v_pk_mul_f32 v[60:61], v[76:77], v[60:61] op_sel_hi:[0,1]
	v_lshlrev_b32_e32 v70, 16, v50
	v_and_b32_e32 v71, 0xffff0000, v50
	v_pk_fma_f32 v[52:53], v[54:55], v[52:53], v[60:61] op_sel_hi:[0,1,1]
	v_pk_add_f32 v[60:61], v[52:53], v[70:71]
	v_pk_mul_f32 v[52:53], v[76:77], v[68:69] op_sel_hi:[0,1]
	v_lshlrev_b32_e32 v50, 16, v51
	v_and_b32_e32 v51, 0xffff0000, v51
	v_pk_fma_f32 v[52:53], v[54:55], v[64:65], v[52:53] op_sel_hi:[0,1,1]
	v_cvt_pk_f32_fp8_e32 v[64:65], v73
	v_pk_add_f32 v[70:71], v[52:53], v[50:51]
	v_cvt_pk_f32_fp8_e32 v[50:51], v72
	v_cvt_pk_f32_fp8_sdwa v[68:69], v73 src0_sel:WORD_1
	v_cvt_pk_f32_fp8_sdwa v[52:53], v72 src0_sel:WORD_1
	v_pk_mul_f32 v[64:65], v[76:77], v[64:65] op_sel_hi:[0,1]
	v_lshlrev_b32_e32 v72, 16, v48
	v_and_b32_e32 v73, 0xffff0000, v48
	v_pk_fma_f32 v[50:51], v[54:55], v[50:51], v[64:65] op_sel_hi:[0,1,1]
	v_pk_add_f32 v[64:65], v[50:51], v[72:73]
	v_pk_mul_f32 v[50:51], v[76:77], v[68:69] op_sel_hi:[0,1]
	v_lshlrev_b32_e32 v48, 16, v49
	v_and_b32_e32 v49, 0xffff0000, v49
	v_pk_fma_f32 v[50:51], v[54:55], v[52:53], v[50:51] op_sel_hi:[0,1,1]
	v_cvt_pk_f32_fp8_e32 v[52:53], v75
	v_pk_add_f32 v[72:73], v[50:51], v[48:49]
	v_cvt_pk_f32_fp8_e32 v[48:49], v74
	v_cvt_pk_f32_fp8_sdwa v[50:51], v74 src0_sel:WORD_1
	v_cvt_pk_f32_fp8_sdwa v[74:75], v75 src0_sel:WORD_1
; template <int MODE, bool W8 = false>
; __device__ __forceinline__ void norm_rows(const Ctx& C, const void* src, bf16* xdst, const unsigned char* YS8, const int* srow, const float* gate, const float* gain, bf16* XN, float* outf, unsigned char* XN8 = nullptr) {
;     ...
;                 for (int j = 0; j < 8; ++j) { const unsigned a = ya[q][j], b = yb[q][j];
;                     const f32x2_m a01 = __builtin_amdgcn_cvt_pk_f32_fp8((int)a, false), a23 = __builtin_amdgcn_cvt_pk_f32_fp8((int)a, true), b01 = __builtin_amdgcn_cvt_pk_f32_fp8((int)b, false), b23 = __builtin_amdgcn_cvt_pk_f32_fp8((int)b, true);
;                     v[q][j].x += h0[q] * a01.x + h1[q] * b01.x; v[q][j].y += h0[q] * a01.y + h1[q] * b01.y; v[q][j].z += h0[q] * a23.x + h1[q] * b23.x; v[q][j].w += h0[q] * a23.y + h1[q] * b23.y; } }
;             float ss = 0.f;
; #pragma unroll
;             for (int j = 0; j < 8; ++j) ss += (v[q][j].x * v[q][j].x + v[q][j].y * v[q][j].y) + (v[q][j].z * v[q][j].z + v[q][j].w * v[q][j].w);
;             const float rstd = 1.0f / sqrtf(wave_sum(ss) * (1.0f / DM) + RMS_EPS);
	v_pk_mul_f32 v[52:53], v[76:77], v[52:53] op_sel_hi:[0,1]
	v_lshlrev_b32_e32 v68, 16, v44
	v_and_b32_e32 v69, 0xffff0000, v44
	v_pk_fma_f32 v[48:49], v[54:55], v[48:49], v[52:53] op_sel_hi:[0,1,1]
	v_pk_add_f32 v[68:69], v[48:49], v[68:69]
	v_pk_mul_f32 v[48:49], v[76:77], v[74:75] op_sel_hi:[0,1]
	v_lshlrev_b32_e32 v44, 16, v45
	v_and_b32_e32 v45, 0xffff0000, v45
	v_pk_fma_f32 v[48:49], v[54:55], v[50:51], v[48:49] op_sel_hi:[0,1,1]
	v_cvt_pk_f32_fp8_e32 v[50:51], v79
	v_pk_add_f32 v[74:75], v[48:49], v[44:45]
	v_cvt_pk_f32_fp8_e32 v[44:45], v78
	v_cvt_pk_f32_fp8_sdwa v[52:53], v79 src0_sel:WORD_1
	v_cvt_pk_f32_fp8_sdwa v[48:49], v78 src0_sel:WORD_1
	v_pk_mul_f32 v[50:51], v[76:77], v[50:51] op_sel_hi:[0,1]
	v_pk_fma_f32 v[44:45], v[54:55], v[44:45], v[50:51] op_sel_hi:[0,1,1]
	v_pk_mul_f32 v[50:51], v[76:77], v[52:53] op_sel_hi:[0,1]
	v_lshlrev_b32_e32 v78, 16, v46
	v_and_b32_e32 v79, 0xffff0000, v46
	v_lshlrev_b32_e32 v46, 16, v47
	v_and_b32_e32 v47, 0xffff0000, v47
	v_pk_fma_f32 v[48:49], v[54:55], v[48:49], v[50:51] op_sel_hi:[0,1,1]
	v_cvt_pk_f32_fp8_e32 v[52:53], v98
	v_pk_add_f32 v[44:45], v[44:45], v[78:79]
	v_pk_add_f32 v[46:47], v[48:49], v[46:47]
	v_cvt_pk_f32_fp8_e32 v[48:49], v97
	v_cvt_pk_f32_fp8_sdwa v[78:79], v98 src0_sel:WORD_1
	v_cvt_pk_f32_fp8_sdwa v[50:51], v97 src0_sel:WORD_1
	v_pk_mul_f32 v[52:53], v[76:77], v[52:53] op_sel_hi:[0,1]
	v_pk_fma_f32 v[48:49], v[54:55], v[48:49], v[52:53] op_sel_hi:[0,1,1]
	v_pk_mul_f32 v[52:53], v[76:77], v[78:79] op_sel_hi:[0,1]
	v_lshlrev_b32_e32 v98, 16, v6
	v_lshlrev_b32_e32 v6, 16, v7
	v_and_b32_e32 v7, 0xffff0000, v7
	v_pk_fma_f32 v[50:51], v[54:55], v[50:51], v[52:53] op_sel_hi:[0,1,1]
	v_cvt_pk_f32_fp8_e32 v[52:53], v101
	v_pk_add_f32 v[50:51], v[50:51], v[6:7]
	v_cvt_pk_f32_fp8_e32 v[6:7], v100
	v_pk_add_f32 v[48:49], v[48:49], v[98:99]
	v_cvt_pk_f32_fp8_sdwa v[98:99], v101 src0_sel:WORD_1
	v_cvt_pk_f32_fp8_sdwa v[78:79], v100 src0_sel:WORD_1
	v_pk_mul_f32 v[52:53], v[76:77], v[52:53] op_sel_hi:[0,1]
	v_lshlrev_b32_e32 v100, 16, v4
	v_and_b32_e32 v101, 0xffff0000, v4
	v_pk_fma_f32 v[6:7], v[54:55], v[6:7], v[52:53] op_sel_hi:[0,1,1]
	v_pk_add_f32 v[52:53], v[6:7], v[100:101]
	v_pk_mul_f32 v[6:7], v[76:77], v[98:99] op_sel_hi:[0,1]
	v_lshlrev_b32_e32 v4, 16, v5
	v_and_b32_e32 v5, 0xffff0000, v5
	v_pk_fma_f32 v[6:7], v[54:55], v[78:79], v[6:7] op_sel_hi:[0,1,1]
	v_pk_add_f32 v[54:55], v[6:7], v[4:5]
	v_mov_b32_e32 v6, v57
	v_mov_b32_e32 v7, v59
	v_mov_b32_e32 v4, v56
	v_mov_b32_e32 v5, v58
	v_pk_mul_f32 v[6:7], v[6:7], v[6:7]
	v_mov_b32_e32 v78, v63
	v_mov_b32_e32 v79, v67
	v_pk_fma_f32 v[4:5], v[4:5], v[4:5], v[6:7]
	v_mov_b32_e32 v6, v62
	v_mov_b32_e32 v7, v66
	v_pk_mul_f32 v[78:79], v[78:79], v[78:79]
	v_mul_f32_e32 v76, v65, v65
	v_pk_fma_f32 v[6:7], v[6:7], v[6:7], v[78:79]
	v_mov_b32_e32 v78, v61
	v_mov_b32_e32 v79, v71
	v_pk_add_f32 v[4:5], v[4:5], v[6:7]
	v_mov_b32_e32 v6, v60
	v_mov_b32_e32 v7, v70
	v_pk_mul_f32 v[78:79], v[78:79], v[78:79]
	v_pk_add_f32 v[4:5], v[4:5], v[4:5] op_sel:[0,1] op_sel_hi:[1,0]
	v_pk_fma_f32 v[6:7], v[6:7], v[6:7], v[78:79]
	v_pk_fma_f32 v[78:79], v[64:65], v[64:65], v[76:77] op_sel_hi:[1,1,0]
	v_mul_f32_e32 v76, v73, v73
	v_pk_add_f32 v[6:7], v[6:7], v[6:7] op_sel:[0,1] op_sel_hi:[1,0]
	v_pk_fma_f32 v[98:99], v[72:73], v[72:73], v[76:77] op_sel_hi:[1,1,0]
	v_pk_mul_f32 v[100:101], v[68:69], v[68:69]
	v_pk_mul_f32 v[102:103], v[74:75], v[74:75]
	v_mov_b32_e32 v5, v100
	v_mov_b32_e32 v7, v101
	v_mov_b32_e32 v79, v102
	v_mov_b32_e32 v99, v103
	v_pk_add_f32 v[4:5], v[4:5], v[6:7]
	v_pk_add_f32 v[6:7], v[78:79], v[98:99]
	v_mov_b32_e32 v78, v45
	v_mov_b32_e32 v79, v47
	v_pk_add_f32 v[4:5], v[4:5], v[6:7]
	v_mov_b32_e32 v6, v44
	v_mov_b32_e32 v7, v46
	v_pk_mul_f32 v[78:79], v[78:79], v[78:79]
	v_mul_f32_e32 v76, v49, v49
	v_pk_fma_f32 v[6:7], v[6:7], v[6:7], v[78:79]
	v_pk_fma_f32 v[78:79], v[48:49], v[48:49], v[76:77] op_sel_hi:[1,1,0]
	v_mul_f32_e32 v76, v51, v51
	v_pk_add_f32 v[4:5], v[4:5], v[4:5] op_sel:[0,1] op_sel_hi:[1,0]
	v_pk_add_f32 v[6:7], v[6:7], v[6:7] op_sel:[0,1] op_sel_hi:[1,0]
	v_pk_fma_f32 v[98:99], v[50:51], v[50:51], v[76:77] op_sel_hi:[1,1,0]
	v_pk_mul_f32 v[100:101], v[52:53], v[52:53]
	v_pk_mul_f32 v[102:103], v[54:55], v[54:55]
	v_mov_b32_e32 v5, v100
	v_mov_b32_e32 v7, v101
	v_mov_b32_e32 v79, v102
	v_mov_b32_e32 v99, v103
	v_pk_add_f32 v[4:5], v[4:5], v[6:7]
	v_pk_add_f32 v[6:7], v[78:79], v[98:99]
	s_nop 0
	v_pk_add_f32 v[4:5], v[4:5], v[6:7]
	s_nop 0
	v_add_f32_e32 v4, v4, v5
	ds_bpermute_b32 v5, v3, v4
	s_waitcnt lgkmcnt(0)
	v_add_f32_e32 v4, v4, v5
	ds_bpermute_b32 v5, v27, v4
	s_waitcnt lgkmcnt(0)
	v_add_f32_e32 v4, v4, v5
	ds_bpermute_b32 v5, v77, v4
	s_waitcnt lgkmcnt(0)
	v_add_f32_e32 v4, v4, v5
	ds_bpermute_b32 v5, v80, v4
	s_waitcnt lgkmcnt(0)
	v_add_f32_e32 v4, v4, v5
	ds_bpermute_b32 v5, v81, v4
	s_waitcnt lgkmcnt(0)
	v_add_f32_e32 v4, v4, v5
	ds_bpermute_b32 v5, v82, v4
	s_waitcnt lgkmcnt(0)
; #define GAS __attribute__((address_space(1)))
; __device__ __forceinline__ unsigned pk2(float lo, float hi) { f32x2_m v = {lo, hi}; bf16x2_m b = __builtin_convertvector(v, bf16x2_m); return __builtin_bit_cast(unsigned, b); }
; template <int MODE, bool W8 = false>
; __device__ __forceinline__ void norm_rows(const Ctx& C, const void* src, bf16* xdst, const unsigned char* YS8, const int* srow, const float* gate, const float* gain, bf16* XN, float* outf, unsigned char* XN8 = nullptr) {
;     ...
;                 for (int j = 0; j < 8; ++j) { const unsigned a = ya[q][j], b = yb[q][j];
;                     const f32x2_m a01 = __builtin_amdgcn_cvt_pk_f32_fp8((int)a, false), a23 = __builtin_amdgcn_cvt_pk_f32_fp8((int)a, true), b01 = __builtin_amdgcn_cvt_pk_f32_fp8((int)b, false), b23 = __builtin_amdgcn_cvt_pk_f32_fp8((int)b, true);
;                     v[q][j].x += h0[q] * a01.x + h1[q] * b01.x; v[q][j].y += h0[q] * a01.y + h1[q] * b01.y; v[q][j].z += h0[q] * a23.x + h1[q] * b23.x; v[q][j].w += h0[q] * a23.y + h1[q] * b23.y; } }
;             float ss = 0.f;
; #pragma unroll
;             for (int j = 0; j < 8; ++j) ss += (v[q][j].x * v[q][j].x + v[q][j].y * v[q][j].y) + (v[q][j].z * v[q][j].z + v[q][j].w * v[q][j].w);
;             const float rstd = 1.0f / sqrtf(wave_sum(ss) * (1.0f / DM) + RMS_EPS);
;             if (MODE == 1) { GAS v2u* xo = (GAS v2u*)(xdst + (size_t)m * DM) + C.lane;
; #pragma unroll
;                 for (int j = 0; j < 8; ++j) { v2u w; w.x = pk2(v[q][j].x, v[q][j].y); w.y = pk2(v[q][j].z, v[q][j].w); xo[64 * j] = w; } }
;             const GAS f32x4* gg = (const GAS f32x4*)gain + C.lane;
;             if (MODE <= 1) { GAS v2u* o = (GAS v2u*)(XN + (size_t)m * DM) + C.lane;
; #pragma unroll
;                 for (int j = 0; j < 8; ++j) { const f32x4 g = gg[64 * j]; const f32x4 y = v[q][j] * rstd * g; v2u w; w.x = pk2(y.x, y.y); w.y = pk2(y.z, y.w); o[64 * j] = w;
;                     if constexpr (W8) ((GAS unsigned*)(XN8 + (size_t)m * DM) + C.lane)[64 * j] = pk4_fp8m(y.x * SXN, y.y * SXN, y.z * SXN, y.w * SXN); } }
;             else { GAS f32x4* o = (GAS f32x4*)(outf + (size_t)m * DM) + C.lane;
; #pragma unroll
;                 for (int j = 0; j < 8; ++j) { const f32x4 g = gg[64 * j]; o[64 * j] = v[q][j] * rstd * g; } } }
	v_add_f32_e32 v4, v4, v5
	v_fmamk_f32 v4, v4, 0x3a000000, v212
	v_cmp_gt_f32_e32 vcc, s30, v4
	v_mul_f32_e32 v5, 0x4f800000, v4
	s_nop 0
	v_cndmask_b32_e32 v4, v4, v5, vcc
	v_sqrt_f32_e32 v5, v4
	s_nop 0
	v_add_u32_e32 v6, -1, v5
	v_fma_f32 v7, -v6, v5, v4
	v_cmp_ge_f32_e64 s[2:3], 0, v7
	v_add_u32_e32 v7, 1, v5
	s_nop 0
	v_cndmask_b32_e64 v6, v5, v6, s[2:3]
	v_fma_f32 v5, -v7, v5, v4
	v_cmp_lt_f32_e64 s[2:3], 0, v5
	s_nop 1
	v_cndmask_b32_e64 v5, v6, v7, s[2:3]
	v_mul_f32_e32 v6, 0x37800000, v5
	v_cndmask_b32_e32 v5, v5, v6, vcc
	v_cmp_class_f32_e32 vcc, v4, v211
	s_nop 1
	v_cndmask_b32_e32 v4, v5, v4, vcc
	v_div_scale_f32 v5, s[2:3], v4, v4, 1.0
	v_rcp_f32_e32 v6, v5
	s_nop 0
	v_fma_f32 v7, -v5, v6, 1.0
	v_fmac_f32_e32 v6, v7, v6
	v_div_scale_f32 v7, vcc, 1.0, v4, 1.0
	v_mul_f32_e32 v76, v7, v6
	v_fma_f32 v78, -v5, v76, v7
	v_fmac_f32_e32 v76, v78, v6
	v_fma_f32 v5, -v5, v76, v7
	v_div_fmas_f32 v5, v5, v6, v76
	v_div_fixup_f32 v76, v5, v4, 1.0
	v_pk_mul_f32 v[56:57], v[56:57], v[76:77] op_sel_hi:[1,0]
	v_pk_mul_f32 v[62:63], v[62:63], v[76:77] op_sel_hi:[1,0]
	v_lshl_add_u64 v[78:79], s[20:21], 0, v[0:1]
	v_pk_mul_f32 v[58:59], v[58:59], v[76:77] op_sel_hi:[1,0]
	v_pk_mul_f32 v[46:47], v[46:47], v[76:77] op_sel_hi:[1,0]
	v_pk_mul_f32 v[44:45], v[44:45], v[76:77] op_sel_hi:[1,0]
	v_pk_mul_f32 v[6:7], v[162:163], v[62:63]
	v_pk_mul_f32 v[4:5], v[160:161], v[56:57]
	global_store_dwordx4 v[78:79], v[4:7], off
	s_nop 1
	v_pk_mul_f32 v[56:57], v[66:67], v[76:77] op_sel_hi:[1,0]
	v_lshlrev_b32_e32 v62, 16, v24
	v_and_b32_e32 v63, 0xffff0000, v24
	v_lshlrev_b32_e32 v24, 16, v25
	v_and_b32_e32 v25, 0xffff0000, v25
	v_pk_mul_f32 v[4:5], v[164:165], v[58:59]
	v_pk_mul_f32 v[6:7], v[166:167], v[56:57]
	global_store_dwordx4 v[78:79], v[4:7], off offset:1024
	s_nop 1
	v_pk_mul_f32 v[56:57], v[70:71], v[76:77] op_sel_hi:[1,0]
	v_pk_mul_f32 v[58:59], v[60:61], v[76:77] op_sel_hi:[1,0]
	v_lshlrev_b32_e32 v60, 16, v30
	v_and_b32_e32 v61, 0xffff0000, v30
	v_lshlrev_b32_e32 v30, 16, v31
	v_and_b32_e32 v31, 0xffff0000, v31
	v_pk_mul_f32 v[4:5], v[168:169], v[58:59]
	v_pk_mul_f32 v[6:7], v[170:171], v[56:57]
	global_store_dwordx4 v[78:79], v[4:7], off offset:2048
	s_nop 1
	v_pk_mul_f32 v[56:57], v[72:73], v[76:77] op_sel_hi:[1,0]
	v_pk_mul_f32 v[58:59], v[64:65], v[76:77] op_sel_hi:[1,0]
	v_pk_mul_f32 v[6:7], v[174:175], v[56:57]
	v_pk_mul_f32 v[4:5], v[172:173], v[58:59]
	global_store_dwordx4 v[78:79], v[4:7], off offset:3072
	s_nop 1
	v_pk_mul_f32 v[56:57], v[74:75], v[76:77] op_sel_hi:[1,0]
	v_pk_mul_f32 v[58:59], v[68:69], v[76:77] op_sel_hi:[1,0]
	v_pk_mul_f32 v[6:7], v[178:179], v[56:57]
	v_add_co_u32_e32 v56, vcc, s27, v78
	v_pk_mul_f32 v[4:5], v[176:177], v[58:59]
	s_nop 0
	v_addc_co_u32_e32 v57, vcc, 0, v79, vcc
	global_store_dwordx4 v[56:57], v[4:7], off
	s_nop 1
	v_lshlrev_b32_e32 v58, 16, v32
	v_and_b32_e32 v59, 0xffff0000, v32
	v_lshlrev_b32_e32 v32, 16, v33
	v_and_b32_e32 v33, 0xffff0000, v33
	v_pk_mul_f32 v[4:5], v[180:181], v[44:45]
	v_pk_mul_f32 v[6:7], v[182:183], v[46:47]
	global_store_dwordx4 v[56:57], v[4:7], off offset:1024
	s_nop 1
	v_pk_mul_f32 v[44:45], v[50:51], v[76:77] op_sel_hi:[1,0]
	v_pk_mul_f32 v[46:47], v[48:49], v[76:77] op_sel_hi:[1,0]
	v_lshlrev_b32_e32 v48, 16, v42
	v_and_b32_e32 v49, 0xffff0000, v42
	v_lshlrev_b32_e32 v50, 16, v40
	v_and_b32_e32 v51, 0xffff0000, v40
	v_pk_mul_f32 v[4:5], v[184:185], v[46:47]
	v_pk_mul_f32 v[6:7], v[186:187], v[44:45]
	global_store_dwordx4 v[56:57], v[4:7], off offset:2048
	s_nop 1
	v_pk_mul_f32 v[44:45], v[54:55], v[76:77] op_sel_hi:[1,0]
	v_pk_mul_f32 v[46:47], v[52:53], v[76:77] op_sel_hi:[1,0]
	v_lshlrev_b32_e32 v52, 16, v38
	v_and_b32_e32 v53, 0xffff0000, v38
	v_lshlrev_b32_e32 v54, 16, v36
	v_and_b32_e32 v55, 0xffff0000, v36
	v_pk_mul_f32 v[4:5], v[188:189], v[46:47]
	v_pk_mul_f32 v[6:7], v[190:191], v[44:45]
	s_waitcnt vmcnt(7)
	v_cvt_pk_f32_fp8_e32 v[44:45], v95
	global_store_dwordx4 v[56:57], v[4:7], off offset:3072
	s_nop 1
	v_cvt_pk_f32_fp8_sdwa v[46:47], v95 src0_sel:WORD_1
	v_lshlrev_b32_e32 v56, 16, v34
	v_cvt_pk_f32_fp8_e32 v[4:5], v96
	v_cvt_pk_f32_fp8_sdwa v[6:7], v96 src0_sel:WORD_1
	v_pk_mul_f32 v[44:45], v[28:29], v[44:45] op_sel_hi:[0,1]
	v_and_b32_e32 v57, 0xffff0000, v34
	v_pk_fma_f32 v[4:5], v[26:27], v[4:5], v[44:45] op_sel_hi:[0,1,1]
	v_pk_add_f32 v[44:45], v[4:5], v[48:49]
	v_lshlrev_b32_e32 v4, 16, v43
	v_and_b32_e32 v5, 0xffff0000, v43
	v_pk_mul_f32 v[42:43], v[28:29], v[46:47] op_sel_hi:[0,1]
	v_pk_fma_f32 v[6:7], v[26:27], v[6:7], v[42:43] op_sel_hi:[0,1,1]
	v_cvt_pk_f32_fp8_e32 v[42:43], v93
	v_pk_add_f32 v[46:47], v[6:7], v[4:5]
	v_cvt_pk_f32_fp8_e32 v[4:5], v94
	v_cvt_pk_f32_fp8_sdwa v[48:49], v93 src0_sel:WORD_1
	v_cvt_pk_f32_fp8_sdwa v[6:7], v94 src0_sel:WORD_1
	v_pk_mul_f32 v[42:43], v[28:29], v[42:43] op_sel_hi:[0,1]
	v_pk_fma_f32 v[4:5], v[26:27], v[4:5], v[42:43] op_sel_hi:[0,1,1]
	v_pk_add_f32 v[42:43], v[4:5], v[50:51]
	v_lshlrev_b32_e32 v4, 16, v41
	v_and_b32_e32 v5, 0xffff0000, v41
	v_pk_mul_f32 v[40:41], v[28:29], v[48:49] op_sel_hi:[0,1]
	v_pk_fma_f32 v[6:7], v[26:27], v[6:7], v[40:41] op_sel_hi:[0,1,1]
	v_cvt_pk_f32_fp8_e32 v[40:41], v91
	v_pk_add_f32 v[48:49], v[6:7], v[4:5]
	v_cvt_pk_f32_fp8_e32 v[4:5], v92
	v_cvt_pk_f32_fp8_sdwa v[50:51], v91 src0_sel:WORD_1
	v_cvt_pk_f32_fp8_sdwa v[6:7], v92 src0_sel:WORD_1
	v_pk_mul_f32 v[40:41], v[28:29], v[40:41] op_sel_hi:[0,1]
	v_pk_fma_f32 v[4:5], v[26:27], v[4:5], v[40:41] op_sel_hi:[0,1,1]
	v_pk_add_f32 v[40:41], v[4:5], v[52:53]
	v_lshlrev_b32_e32 v4, 16, v39
	v_and_b32_e32 v5, 0xffff0000, v39
	v_pk_mul_f32 v[38:39], v[28:29], v[50:51] op_sel_hi:[0,1]
	v_pk_fma_f32 v[6:7], v[26:27], v[6:7], v[38:39] op_sel_hi:[0,1,1]
; template <int MODE, bool W8 = false>
; __device__ __forceinline__ void norm_rows(const Ctx& C, const void* src, bf16* xdst, const unsigned char* YS8, const int* srow, const float* gate, const float* gain, bf16* XN, float* outf, unsigned char* XN8 = nullptr) {
;     ...
;                 for (int j = 0; j < 8; ++j) { const unsigned a = ya[q][j], b = yb[q][j];
;                     const f32x2_m a01 = __builtin_amdgcn_cvt_pk_f32_fp8((int)a, false), a23 = __builtin_amdgcn_cvt_pk_f32_fp8((int)a, true), b01 = __builtin_amdgcn_cvt_pk_f32_fp8((int)b, false), b23 = __builtin_amdgcn_cvt_pk_f32_fp8((int)b, true);
;                     v[q][j].x += h0[q] * a01.x + h1[q] * b01.x; v[q][j].y += h0[q] * a01.y + h1[q] * b01.y; v[q][j].z += h0[q] * a23.x + h1[q] * b23.x; v[q][j].w += h0[q] * a23.y + h1[q] * b23.y; } }
;             float ss = 0.f;
; #pragma unroll
;             for (int j = 0; j < 8; ++j) ss += (v[q][j].x * v[q][j].x + v[q][j].y * v[q][j].y) + (v[q][j].z * v[q][j].z + v[q][j].w * v[q][j].w);
;             const float rstd = 1.0f / sqrtf(wave_sum(ss) * (1.0f / DM) + RMS_EPS);
	v_cvt_pk_f32_fp8_e32 v[38:39], v89
	v_pk_add_f32 v[50:51], v[6:7], v[4:5]
	v_cvt_pk_f32_fp8_e32 v[4:5], v90
	v_cvt_pk_f32_fp8_sdwa v[52:53], v89 src0_sel:WORD_1
	v_cvt_pk_f32_fp8_sdwa v[6:7], v90 src0_sel:WORD_1
	v_pk_mul_f32 v[38:39], v[28:29], v[38:39] op_sel_hi:[0,1]
	v_pk_fma_f32 v[4:5], v[26:27], v[4:5], v[38:39] op_sel_hi:[0,1,1]
	v_pk_add_f32 v[38:39], v[4:5], v[54:55]
	v_lshlrev_b32_e32 v4, 16, v37
	v_and_b32_e32 v5, 0xffff0000, v37
	v_pk_mul_f32 v[36:37], v[28:29], v[52:53] op_sel_hi:[0,1]
	v_pk_fma_f32 v[6:7], v[26:27], v[6:7], v[36:37] op_sel_hi:[0,1,1]
	v_cvt_pk_f32_fp8_e32 v[36:37], v87
	v_pk_add_f32 v[52:53], v[6:7], v[4:5]
	v_cvt_pk_f32_fp8_e32 v[4:5], v88
	v_cvt_pk_f32_fp8_sdwa v[54:55], v87 src0_sel:WORD_1
	v_cvt_pk_f32_fp8_sdwa v[6:7], v88 src0_sel:WORD_1
	v_pk_mul_f32 v[36:37], v[28:29], v[36:37] op_sel_hi:[0,1]
	v_pk_fma_f32 v[4:5], v[26:27], v[4:5], v[36:37] op_sel_hi:[0,1,1]
	v_pk_add_f32 v[36:37], v[4:5], v[56:57]
	v_lshlrev_b32_e32 v4, 16, v35
	v_and_b32_e32 v5, 0xffff0000, v35
	v_pk_mul_f32 v[34:35], v[28:29], v[54:55] op_sel_hi:[0,1]
	v_pk_fma_f32 v[6:7], v[26:27], v[6:7], v[34:35] op_sel_hi:[0,1,1]
	v_cvt_pk_f32_fp8_e32 v[34:35], v85
	v_pk_add_f32 v[54:55], v[6:7], v[4:5]
	v_cvt_pk_f32_fp8_e32 v[4:5], v86
	v_cvt_pk_f32_fp8_sdwa v[56:57], v85 src0_sel:WORD_1
	v_cvt_pk_f32_fp8_sdwa v[6:7], v86 src0_sel:WORD_1
	v_pk_mul_f32 v[34:35], v[28:29], v[34:35] op_sel_hi:[0,1]
	v_pk_fma_f32 v[4:5], v[26:27], v[4:5], v[34:35] op_sel_hi:[0,1,1]
	v_pk_mul_f32 v[34:35], v[28:29], v[56:57] op_sel_hi:[0,1]
	v_pk_fma_f32 v[6:7], v[26:27], v[6:7], v[34:35] op_sel_hi:[0,1,1]
	v_cvt_pk_f32_fp8_e32 v[56:57], v83
	v_pk_add_f32 v[32:33], v[6:7], v[32:33]
	v_cvt_pk_f32_fp8_e32 v[6:7], v84
	v_pk_add_f32 v[4:5], v[4:5], v[58:59]
	v_cvt_pk_f32_fp8_sdwa v[58:59], v83 src0_sel:WORD_1
	v_cvt_pk_f32_fp8_sdwa v[34:35], v84 src0_sel:WORD_1
	v_pk_mul_f32 v[56:57], v[28:29], v[56:57] op_sel_hi:[0,1]
	v_pk_fma_f32 v[6:7], v[26:27], v[6:7], v[56:57] op_sel_hi:[0,1,1]
	v_pk_add_f32 v[6:7], v[6:7], v[60:61]
	v_pk_mul_f32 v[56:57], v[28:29], v[58:59] op_sel_hi:[0,1]
	v_cvt_pk_f32_fp8_e32 v[58:59], v17
	v_cvt_pk_f32_fp8_sdwa v[60:61], v17 src0_sel:WORD_1
	v_pk_fma_f32 v[34:35], v[26:27], v[34:35], v[56:57] op_sel_hi:[0,1,1]
	v_cvt_pk_f32_fp8_sdwa v[56:57], v29 src0_sel:WORD_1
	v_pk_add_f32 v[34:35], v[34:35], v[30:31]
	v_cvt_pk_f32_fp8_e32 v[30:31], v29
	v_pk_mul_f32 v[58:59], v[28:29], v[58:59] op_sel_hi:[0,1]
	v_pk_mul_f32 v[28:29], v[28:29], v[60:61] op_sel_hi:[0,1]
	v_pk_fma_f32 v[28:29], v[26:27], v[56:57], v[28:29] op_sel_hi:[0,1,1]
	v_mov_b32_e32 v56, v45
	v_mov_b32_e32 v57, v43
	v_pk_fma_f32 v[30:31], v[26:27], v[30:31], v[58:59] op_sel_hi:[0,1,1]
	v_pk_add_f32 v[24:25], v[28:29], v[24:25]
	v_mov_b32_e32 v28, v44
	v_mov_b32_e32 v29, v42
	v_pk_mul_f32 v[56:57], v[56:57], v[56:57]
	v_mov_b32_e32 v58, v47
	v_mov_b32_e32 v59, v49
	v_pk_fma_f32 v[28:29], v[28:29], v[28:29], v[56:57]
	v_mov_b32_e32 v56, v46
	v_mov_b32_e32 v57, v48
	v_pk_mul_f32 v[58:59], v[58:59], v[58:59]
	v_mul_f32_e32 v26, v39, v39
	v_pk_fma_f32 v[56:57], v[56:57], v[56:57], v[58:59]
	v_mov_b32_e32 v58, v41
	v_mov_b32_e32 v59, v51
	v_pk_add_f32 v[28:29], v[28:29], v[56:57]
	v_mov_b32_e32 v56, v40
	v_mov_b32_e32 v57, v50
	v_pk_mul_f32 v[58:59], v[58:59], v[58:59]
	v_pk_add_f32 v[30:31], v[30:31], v[62:63]
	v_pk_fma_f32 v[56:57], v[56:57], v[56:57], v[58:59]
	v_pk_fma_f32 v[58:59], v[38:39], v[38:39], v[26:27] op_sel_hi:[1,1,0]
	v_mul_f32_e32 v26, v53, v53
	v_pk_add_f32 v[28:29], v[28:29], v[28:29] op_sel:[0,1] op_sel_hi:[1,0]
	v_pk_add_f32 v[56:57], v[56:57], v[56:57] op_sel:[0,1] op_sel_hi:[1,0]
	v_pk_fma_f32 v[60:61], v[52:53], v[52:53], v[26:27] op_sel_hi:[1,1,0]
	v_pk_mul_f32 v[62:63], v[36:37], v[36:37]
	v_pk_mul_f32 v[64:65], v[54:55], v[54:55]
	v_mov_b32_e32 v29, v62
	v_mov_b32_e32 v57, v63
	v_mov_b32_e32 v59, v64
	v_mov_b32_e32 v61, v65
	v_pk_add_f32 v[28:29], v[28:29], v[56:57]
	v_pk_add_f32 v[56:57], v[58:59], v[60:61]
	v_mov_b32_e32 v58, v5
	v_mov_b32_e32 v59, v33
	v_pk_add_f32 v[28:29], v[28:29], v[56:57]
	v_mov_b32_e32 v56, v4
	v_mov_b32_e32 v57, v32
	v_pk_mul_f32 v[58:59], v[58:59], v[58:59]
	v_mul_f32_e32 v26, v7, v7
	v_pk_fma_f32 v[56:57], v[56:57], v[56:57], v[58:59]
	v_pk_fma_f32 v[58:59], v[6:7], v[6:7], v[26:27] op_sel_hi:[1,1,0]
	v_mul_f32_e32 v26, v35, v35
	v_pk_add_f32 v[28:29], v[28:29], v[28:29] op_sel:[0,1] op_sel_hi:[1,0]
	v_pk_add_f32 v[56:57], v[56:57], v[56:57] op_sel:[0,1] op_sel_hi:[1,0]
	v_pk_fma_f32 v[60:61], v[34:35], v[34:35], v[26:27] op_sel_hi:[1,1,0]
	v_pk_mul_f32 v[62:63], v[30:31], v[30:31]
	v_pk_mul_f32 v[64:65], v[24:25], v[24:25]
	v_mov_b32_e32 v29, v62
	v_mov_b32_e32 v57, v63
	v_mov_b32_e32 v59, v64
	v_mov_b32_e32 v61, v65
	v_pk_add_f32 v[28:29], v[28:29], v[56:57]
	v_pk_add_f32 v[56:57], v[58:59], v[60:61]
	s_nop 0
	v_pk_add_f32 v[28:29], v[28:29], v[56:57]
	s_nop 0
	v_add_f32_e32 v17, v28, v29
	ds_bpermute_b32 v26, v3, v17
	s_waitcnt lgkmcnt(0)
; #define GAS __attribute__((address_space(1)))
; __device__ __forceinline__ unsigned pk2(float lo, float hi) { f32x2_m v = {lo, hi}; bf16x2_m b = __builtin_convertvector(v, bf16x2_m); return __builtin_bit_cast(unsigned, b); }
; template <int MODE, bool W8 = false>
; __device__ __forceinline__ void norm_rows(const Ctx& C, const void* src, bf16* xdst, const unsigned char* YS8, const int* srow, const float* gate, const float* gain, bf16* XN, float* outf, unsigned char* XN8 = nullptr) {
;     ...
;     for (int m0 = C.gw; m0 < T; m0 += NR * C.NGW) {
;     ...
;             const float rstd = 1.0f / sqrtf(wave_sum(ss) * (1.0f / DM) + RMS_EPS);
;             if (MODE == 1) { GAS v2u* xo = (GAS v2u*)(xdst + (size_t)m * DM) + C.lane;
; #pragma unroll
;                 for (int j = 0; j < 8; ++j) { v2u w; w.x = pk2(v[q][j].x, v[q][j].y); w.y = pk2(v[q][j].z, v[q][j].w); xo[64 * j] = w; } }
;             const GAS f32x4* gg = (const GAS f32x4*)gain + C.lane;
;             if (MODE <= 1) { GAS v2u* o = (GAS v2u*)(XN + (size_t)m * DM) + C.lane;
; #pragma unroll
;                 for (int j = 0; j < 8; ++j) { const f32x4 g = gg[64 * j]; const f32x4 y = v[q][j] * rstd * g; v2u w; w.x = pk2(y.x, y.y); w.y = pk2(y.z, y.w); o[64 * j] = w;
;                     if constexpr (W8) ((GAS unsigned*)(XN8 + (size_t)m * DM) + C.lane)[64 * j] = pk4_fp8m(y.x * SXN, y.y * SXN, y.z * SXN, y.w * SXN); } }
;             else { GAS f32x4* o = (GAS f32x4*)(outf + (size_t)m * DM) + C.lane;
; #pragma unroll
;                 for (int j = 0; j < 8; ++j) { const f32x4 g = gg[64 * j]; o[64 * j] = v[q][j] * rstd * g; } } }
	v_add_f32_e32 v17, v17, v26
	ds_bpermute_b32 v26, v27, v17
	s_waitcnt lgkmcnt(0)
	v_add_f32_e32 v17, v17, v26
	ds_bpermute_b32 v26, v77, v17
	s_waitcnt lgkmcnt(0)
	v_add_f32_e32 v17, v17, v26
	ds_bpermute_b32 v26, v80, v17
	s_waitcnt lgkmcnt(0)
	v_add_f32_e32 v17, v17, v26
	ds_bpermute_b32 v26, v81, v17
	s_waitcnt lgkmcnt(0)
	v_add_f32_e32 v17, v17, v26
	ds_bpermute_b32 v26, v82, v17
	s_waitcnt lgkmcnt(0)
	v_add_f32_e32 v17, v17, v26
	v_fmamk_f32 v17, v17, 0x3a000000, v212
	v_cmp_gt_f32_e32 vcc, s30, v17
	v_mul_f32_e32 v26, 0x4f800000, v17
	s_nop 0
	v_cndmask_b32_e32 v17, v17, v26, vcc
	v_sqrt_f32_e32 v26, v17
	s_nop 0
	v_add_u32_e32 v28, -1, v26
	v_fma_f32 v29, -v28, v26, v17
	v_cmp_ge_f32_e64 s[2:3], 0, v29
	v_add_u32_e32 v29, 1, v26
	s_nop 0
	v_cndmask_b32_e64 v28, v26, v28, s[2:3]
	v_fma_f32 v26, -v29, v26, v17
	v_cmp_lt_f32_e64 s[2:3], 0, v26
	s_nop 1
	v_cndmask_b32_e64 v26, v28, v29, s[2:3]
	v_mul_f32_e32 v28, 0x37800000, v26
	v_cndmask_b32_e32 v26, v26, v28, vcc
	v_cmp_class_f32_e32 vcc, v17, v211
	s_nop 1
	v_cndmask_b32_e32 v17, v26, v17, vcc
	v_div_scale_f32 v26, s[2:3], v17, v17, 1.0
	v_rcp_f32_e32 v28, v26
	s_nop 0
	v_fma_f32 v29, -v26, v28, 1.0
	v_fmac_f32_e32 v28, v29, v28
	v_div_scale_f32 v29, vcc, 1.0, v17, 1.0
	v_mul_f32_e32 v56, v29, v28
	v_fma_f32 v57, -v26, v56, v29
	v_fmac_f32_e32 v56, v57, v28
	v_fma_f32 v26, -v26, v56, v29
	v_div_fmas_f32 v26, v26, v28, v56
	v_div_fixup_f32 v26, v26, v17, 1.0
	v_pk_mul_f32 v[46:47], v[46:47], v[26:27] op_sel_hi:[1,0]
	v_pk_mul_f32 v[44:45], v[44:45], v[26:27] op_sel_hi:[1,0]
	v_lshl_add_u64 v[28:29], s[12:13], 0, v[0:1]
	v_pk_mul_f32 v[48:49], v[48:49], v[26:27] op_sel_hi:[1,0]
	v_pk_mul_f32 v[42:43], v[42:43], v[26:27] op_sel_hi:[1,0]
	v_pk_mul_f32 v[40:41], v[40:41], v[26:27] op_sel_hi:[1,0]
	v_pk_mul_f32 v[38:39], v[38:39], v[26:27] op_sel_hi:[1,0]
	v_pk_mul_f32 v[36:37], v[36:37], v[26:27] op_sel_hi:[1,0]
	v_pk_mul_f32 v[32:33], v[32:33], v[26:27] op_sel_hi:[1,0]
	v_pk_mul_f32 v[4:5], v[4:5], v[26:27] op_sel_hi:[1,0]
	s_add_u32 s12, s12, 0x2000000
	s_addc_u32 s13, s13, 0
	s_add_u32 s16, s16, 0x1000000
	s_addc_u32 s17, s17, 0
	s_add_u32 s18, s18, 0x1000000
	s_addc_u32 s19, s19, 0
	s_add_u32 s20, s20, 0x2000000
	v_pk_mul_f32 v[24:25], v[24:25], v[26:27] op_sel_hi:[1,0]
	v_pk_mul_f32 v[30:31], v[30:31], v[26:27] op_sel_hi:[1,0]
	s_addc_u32 s21, s21, 0
	s_cmpk_lt_i32 s26, 0x3000
	v_pk_mul_f32 v[44:45], v[160:161], v[44:45]
	v_pk_mul_f32 v[46:47], v[162:163], v[46:47]
	global_store_dwordx4 v[28:29], v[44:47], off
	s_nop 1
	v_pk_mul_f32 v[42:43], v[164:165], v[42:43]
	v_pk_mul_f32 v[44:45], v[166:167], v[48:49]
	global_store_dwordx4 v[28:29], v[42:45], off offset:1024
	s_nop 1
	v_pk_mul_f32 v[46:47], v[50:51], v[26:27] op_sel_hi:[1,0]
	v_pk_mul_f32 v[40:41], v[168:169], v[40:41]
	v_pk_mul_f32 v[42:43], v[170:171], v[46:47]
	global_store_dwordx4 v[28:29], v[40:43], off offset:2048
	s_nop 1
	v_pk_mul_f32 v[44:45], v[52:53], v[26:27] op_sel_hi:[1,0]
	v_pk_mul_f32 v[38:39], v[172:173], v[38:39]
	v_pk_mul_f32 v[40:41], v[174:175], v[44:45]
	global_store_dwordx4 v[28:29], v[38:41], off offset:3072
	s_nop 1
	v_pk_mul_f32 v[42:43], v[54:55], v[26:27] op_sel_hi:[1,0]
	v_add_co_u32_e32 v28, vcc, s27, v28
	v_pk_mul_f32 v[36:37], v[176:177], v[36:37]
	v_pk_mul_f32 v[38:39], v[178:179], v[42:43]
	v_addc_co_u32_e32 v29, vcc, 0, v29, vcc
	global_store_dwordx4 v[28:29], v[36:39], off
	s_nop 1
	v_pk_mul_f32 v[36:37], v[180:181], v[4:5]
	v_pk_mul_f32 v[38:39], v[182:183], v[32:33]
	global_store_dwordx4 v[28:29], v[36:39], off offset:1024
	s_nop 1
	v_pk_mul_f32 v[32:33], v[34:35], v[26:27] op_sel_hi:[1,0]
	v_pk_mul_f32 v[4:5], v[6:7], v[26:27] op_sel_hi:[1,0]
	v_pk_mul_f32 v[6:7], v[186:187], v[32:33]
	v_pk_mul_f32 v[4:5], v[184:185], v[4:5]
	global_store_dwordx4 v[28:29], v[4:7], off offset:2048
	s_nop 1
	v_pk_mul_f32 v[4:5], v[188:189], v[30:31]
	v_pk_mul_f32 v[6:7], v[190:191], v[24:25]
	global_store_dwordx4 v[28:29], v[4:7], off offset:3072
	s_nop 1
	s_cbranch_scc1 .LBB0_1321

; #define GAS __attribute__((address_space(1)))
; __device__ __forceinline__ float bflo(unsigned w) { return __uint_as_float(w << 16); }
; __device__ __forceinline__ float bfhi(unsigned w) { return __uint_as_float(w & 0xffff0000u); }
; template <int MODE, bool W8 = false>
; __device__ __forceinline__ void norm_rows(const Ctx& C, const void* src, bf16* xdst, const unsigned char* YS8, const int* srow, const float* gate, const float* gain, bf16* XN, float* outf, unsigned char* XN8 = nullptr) {
;     ...
;     for (int m0 = C.gw; m0 < T; m0 += NR * C.NGW) {
;         f32x4 v[NR][8]; unsigned ya[NR][8], yb[NR][8]; float h0[NR], h1[NR];
; #pragma unroll
;         for (int q = 0; q < NR; ++q) { const int m = m0 + q * C.NGW;
;             if (MODE == 0) { const GAS f32x4* xr = (const GAS f32x4*)((const float*)src + (size_t)m * DM) + C.lane;
; #pragma unroll
;                 for (int j = 0; j < 8; ++j) v[q][j] = xr[64 * j]; }
;             else { const GAS v2u* xr = (const GAS v2u*)((const bf16*)src + (size_t)m * DM) + C.lane;
; #pragma unroll
;                 for (int j = 0; j < 8; ++j) { const v2u t_ = xr[64 * j]; v[q][j] = (f32x4){bflo(t_.x), bfhi(t_.x), bflo(t_.y), bfhi(t_.y)}; } }
;             if (MODE >= 1) {
;                 h0[q] = gate[2 * m] * (1.0f / SY); h1[q] = gate[2 * m + 1] * (1.0f / SY);
;                 const GAS unsigned* y0 = (const GAS unsigned*)(YS8 + (size_t)srow[2 * m] * DM) + C.lane; const GAS unsigned* y1 = (const GAS unsigned*)(YS8 + (size_t)srow[2 * m + 1] * DM) + C.lane;
; #pragma unroll
;                 for (int j = 0; j < 8; ++j) { ya[q][j] = y0[64 * j]; yb[q][j] = y1[64 * j]; } } }
;     ...
;             const GAS f32x4* gg = (const GAS f32x4*)gain + C.lane;
.LBB0_1323:
	s_andn2_b64 vcc, exec, s[2:3]
	s_mov_b32 s12, 0xf800000
	s_mov_b32 s13, 0x4b800000
	s_brev_b32 s16, 44
	s_mov_b32 s17, 0x49800000
	s_mov_b64 s[18:19], 0x800000
	s_mov_b64 s[20:21], 0x1000000
	s_cbranch_vccnz .LBB0_1327
	s_and_b64 vcc, exec, s[36:37]
	s_cbranch_vccnz .LBB0_1327
	v_and_b32_e32 v0, 64, v215
	v_add_u32_e32 v0, 64, v0
	v_xor_b32_e32 v1, 1, v215
	v_cmp_lt_i32_e32 vcc, v1, v0
	s_load_dwordx2 s[2:3], s[8:9], 0x10
	v_ashrrev_i32_e32 v17, 31, v16
	v_cndmask_b32_e32 v1, v215, v1, vcc
	v_lshlrev_b32_e32 v3, 2, v1
	v_xor_b32_e32 v1, 2, v215
	v_cmp_lt_i32_e32 vcc, v1, v0
	v_lshlrev_b64 v[18:19], 2, v[16:17]
	s_waitcnt lgkmcnt(0)
	v_lshl_add_u64 v[12:13], v[16:17], 4, s[2:3]
	v_cndmask_b32_e32 v1, v215, v1, vcc
	v_lshlrev_b32_e32 v57, 2, v1
	v_xor_b32_e32 v1, 4, v215
	v_cmp_lt_i32_e32 vcc, v1, v0
	s_add_i32 s2, s6, 0x800
	s_ashr_i32 s3, s2, 31
	v_cndmask_b32_e32 v1, v215, v1, vcc
	v_lshlrev_b32_e32 v81, 2, v1
	v_xor_b32_e32 v1, 8, v215
	v_cmp_lt_i32_e32 vcc, v1, v0
	s_lshl_b64 s[10:11], s[2:3], 11
	s_lshl_b64 s[2:3], s[2:3], 12
	v_cndmask_b32_e32 v1, v215, v1, vcc
	v_lshlrev_b32_e32 v82, 2, v1
	v_xor_b32_e32 v1, 16, v215
	v_cmp_lt_i32_e32 vcc, v1, v0
	v_lshlrev_b64 v[20:21], 3, v[16:17]
	s_ashr_i32 s7, s6, 31
	v_cndmask_b32_e32 v1, v215, v1, vcc
	v_lshlrev_b32_e32 v83, 2, v1
	v_xor_b32_e32 v1, 32, v215
	v_cmp_lt_i32_e32 vcc, v1, v0
	v_lshl_add_u64 v[16:17], s[2:3], 0, v[20:21]
	s_lshl_b64 s[2:3], s[6:7], 11
	v_cndmask_b32_e32 v0, v215, v1, vcc
	v_lshlrev_b32_e32 v84, 2, v0
	v_lshl_add_u64 v[0:1], s[0:1], 0, v[18:19]
	s_mov_b64 s[0:1], 0x2000
	v_lshl_add_u64 v[4:5], v[12:13], 0, s[0:1]
	s_mov_b64 s[0:1], 0x3000
	v_lshl_add_u64 v[6:7], v[12:13], 0, s[0:1]
	s_mov_b64 s[0:1], 0x3400
	v_lshl_add_u64 v[8:9], v[12:13], 0, s[0:1]
	s_mov_b64 s[0:1], 0x3800
	v_lshl_add_u64 v[10:11], v[12:13], 0, s[0:1]
	s_mov_b64 s[0:1], 0x3c00
	v_lshl_add_u64 v[14:15], s[10:11], 0, v[18:19]
	v_lshl_add_u64 v[18:19], s[2:3], 0, v[18:19]
	s_lshl_b64 s[2:3], s[6:7], 12
	v_lshl_add_u64 v[12:13], v[12:13], 0, s[0:1]
	s_add_i32 s8, s6, 0xfffff000
	s_lshl_b32 s0, s6, 1
	v_lshl_add_u64 v[20:21], s[2:3], 0, v[20:21]
	global_load_dwordx4 v[160:163], v[4:5], off
	global_load_dwordx4 v[164:167], v[4:5], off offset:1024
	global_load_dwordx4 v[168:171], v[4:5], off offset:2048
	global_load_dwordx4 v[172:175], v[4:5], off offset:3072
	global_load_dwordx4 v[176:179], v[6:7], off
	global_load_dwordx4 v[180:183], v[8:9], off
	global_load_dwordx4 v[184:187], v[10:11], off
	global_load_dwordx4 v[188:191], v[12:13], off
.LBB0_1326:
	s_ashr_i32 s1, s0, 31
	s_lshl_b64 s[2:3], s[0:1], 2
	s_add_u32 s2, s22, s2
	s_addc_u32 s3, s23, s3
	global_load_dwordx2 v[194:195], v2, s[2:3]
	s_ashr_i32 s1, s0, 31
	v_lshl_add_u64 v[52:53], s[4:5], 0, v[20:21]
	s_lshl_b64 s[2:3], s[0:1], 2
	v_add_co_u32_e32 v50, vcc, 0x4b800000, v52
	s_add_u32 s6, s24, s2
	s_nop 0
	v_addc_co_u32_e32 v51, vcc, 0, v53, vcc
	s_addc_u32 s7, s25, s3
	global_load_dwordx2 v[64:65], v[50:51], off
	global_load_dwordx2 v[62:63], v[50:51], off offset:512
	global_load_dwordx2 v[60:61], v[50:51], off offset:1024
	global_load_dwordx2 v[58:59], v[50:51], off offset:1536
	global_load_dwordx2 v[48:49], v[50:51], off offset:2048
	global_load_dwordx2 v[46:47], v[50:51], off offset:2560
	global_load_dwordx2 v[42:43], v[50:51], off offset:3072
	global_load_dwordx2 v[44:45], v[50:51], off offset:3584
	global_load_dwordx2 v[22:23], v2, s[6:7]
	s_add_i32 s6, s0, 1
	s_ashr_i32 s7, s6, 31
	s_add_u32 s2, s22, s2
	s_addc_u32 s3, s23, s3
	v_lshl_add_u64 v[28:29], s[4:5], 0, v[16:17]
	v_add_co_u32_e32 v26, vcc, s13, v28
	v_lshl_add_u64 v[16:17], v[16:17], 0, s[20:21]
	s_nop 0
	v_addc_co_u32_e32 v27, vcc, 0, v29, vcc
	v_lshl_add_u64 v[20:21], v[20:21], 0, s[20:21]
	s_waitcnt vmcnt(8)
	v_lshlrev_b32_e32 v74, 16, v64
	v_and_b32_e32 v75, 0xffff0000, v64
	v_lshlrev_b32_e32 v64, 16, v65
	v_and_b32_e32 v65, 0xffff0000, v65
	s_waitcnt vmcnt(0)
	v_mul_f32_e32 v78, 0x3d800000, v22
	v_mov_b32_e32 v22, v194
	s_lshl_b64 s[2:3], s[6:7], 2
	s_add_u32 s2, s22, s2
	s_addc_u32 s3, s23, s3
	v_mov_b32_e32 v24, v195
	s_add_i32 s2, s0, 0x1000
	s_ashr_i32 s3, s2, 31
	v_mul_f32_e32 v80, 0x3d800000, v23
	s_lshl_b64 s[2:3], s[2:3], 2
	s_add_u32 s6, s24, s2
	s_addc_u32 s7, s25, s3
	s_waitcnt vmcnt(1)
	v_ashrrev_i32_e32 v23, 31, v22
	v_lshlrev_b64 v[22:23], 11, v[22:23]
	v_lshl_add_u64 v[22:23], v[0:1], 0, v[22:23]
	s_waitcnt vmcnt(0)
	v_ashrrev_i32_e32 v25, 31, v24
	v_lshlrev_b64 v[24:25], 11, v[24:25]
	v_lshl_add_u64 v[24:25], v[0:1], 0, v[24:25]
	global_load_dword v70, v[22:23], off
	global_load_dword v72, v[24:25], off
	global_load_dword v76, v[22:23], off offset:256
	global_load_dword v77, v[24:25], off offset:256
	global_load_dword v79, v[22:23], off offset:512
	global_load_dword v100, v[24:25], off offset:512
	global_load_dword v101, v[22:23], off offset:768
	global_load_dword v102, v[24:25], off offset:768
	global_load_dword v103, v[22:23], off offset:1024
	global_load_dword v108, v[24:25], off offset:1024
	global_load_dword v109, v[22:23], off offset:1280
	global_load_dword v110, v[24:25], off offset:1280
	global_load_dword v111, v[22:23], off offset:1536
	global_load_dword v112, v[24:25], off offset:1536
	global_load_dword v113, v[22:23], off offset:1792
	global_load_dword v114, v[24:25], off offset:1792
	global_load_dwordx2 v[40:41], v[26:27], off
	global_load_dwordx2 v[38:39], v[26:27], off offset:512
	global_load_dwordx2 v[36:37], v[26:27], off offset:1024
	global_load_dwordx2 v[34:35], v[26:27], off offset:1536
	global_load_dwordx2 v[32:33], v[26:27], off offset:2048
	global_load_dwordx2 v[30:31], v[26:27], off offset:2560
	global_load_dwordx2 v[22:23], v[26:27], off offset:3072
	global_load_dwordx2 v[24:25], v[26:27], off offset:3584
	global_load_dwordx2 v[54:55], v2, s[6:7]
	s_add_i32 s6, s0, 0x1001
	s_ashr_i32 s7, s6, 31
	s_add_u32 s2, s22, s2
	s_addc_u32 s3, s23, s3
	global_load_dword v66, v2, s[2:3]
	s_lshl_b64 s[2:3], s[6:7], 2
	s_add_u32 s2, s22, s2
	s_addc_u32 s3, s23, s3
	global_load_dword v68, v2, s[2:3]
	s_addk_i32 s8, 0x1000
	s_addk_i32 s0, 0x2000
	s_cmpk_gt_i32 s8, 0x2fff
	s_waitcnt vmcnt(2)
; #define GAS __attribute__((address_space(1)))
; template <int MODE, bool W8 = false>
; __device__ __forceinline__ void norm_rows(const Ctx& C, const void* src, bf16* xdst, const unsigned char* YS8, const int* srow, const float* gate, const float* gain, bf16* XN, float* outf, unsigned char* XN8 = nullptr) {
;     ...
;             if (MODE >= 1) {
;                 h0[q] = gate[2 * m] * (1.0f / SY); h1[q] = gate[2 * m + 1] * (1.0f / SY);
;                 const GAS unsigned* y0 = (const GAS unsigned*)(YS8 + (size_t)srow[2 * m] * DM) + C.lane; const GAS unsigned* y1 = (const GAS unsigned*)(YS8 + (size_t)srow[2 * m + 1] * DM) + C.lane;
; #pragma unroll
;                 for (int j = 0; j < 8; ++j) { ya[q][j] = y0[64 * j]; yb[q][j] = y1[64 * j]; } } }
; #pragma unroll
;         for (int q = 0; q < NR; ++q) { const int m = m0 + q * C.NGW;
;             if (MODE >= 1) {
; #pragma unroll
;                 for (int j = 0; j < 8; ++j) { const unsigned a = ya[q][j], b = yb[q][j];
;                     const f32x2_m a01 = __builtin_amdgcn_cvt_pk_f32_fp8((int)a, false), a23 = __builtin_amdgcn_cvt_pk_f32_fp8((int)a, true), b01 = __builtin_amdgcn_cvt_pk_f32_fp8((int)b, false), b23 = __builtin_amdgcn_cvt_pk_f32_fp8((int)b, true);
;                     v[q][j].x += h0[q] * a01.x + h1[q] * b01.x; v[q][j].y += h0[q] * a01.y + h1[q] * b01.y; v[q][j].z += h0[q] * a23.x + h1[q] * b23.x; v[q][j].w += h0[q] * a23.y + h1[q] * b23.y; } }
	v_mul_f32_e32 v56, 0x3d800000, v55
	v_mul_f32_e32 v54, 0x3d800000, v54
	s_waitcnt vmcnt(1)
	v_ashrrev_i32_e32 v67, 31, v66
	v_lshlrev_b64 v[66:67], 11, v[66:67]
	v_lshl_add_u64 v[66:67], v[0:1], 0, v[66:67]
	s_waitcnt vmcnt(0)
	v_ashrrev_i32_e32 v69, 31, v68
	v_lshlrev_b64 v[68:69], 11, v[68:69]
	v_lshl_add_u64 v[68:69], v[0:1], 0, v[68:69]
	global_load_dword v99, v[66:67], off
	global_load_dword v98, v[68:69], off
	global_load_dword v97, v[66:67], off offset:256
	global_load_dword v96, v[68:69], off offset:256
	global_load_dword v95, v[66:67], off offset:512
	global_load_dword v94, v[68:69], off offset:512
	global_load_dword v93, v[66:67], off offset:768
	global_load_dword v92, v[68:69], off offset:768
	global_load_dword v91, v[66:67], off offset:1024
	global_load_dword v90, v[68:69], off offset:1024
	global_load_dword v89, v[66:67], off offset:1280
	global_load_dword v88, v[68:69], off offset:1280
	global_load_dword v87, v[66:67], off offset:1536
	global_load_dword v86, v[68:69], off offset:1536
	global_load_dword v85, v[66:67], off offset:1792
	global_load_dword v55, v[68:69], off offset:1792
	v_cvt_pk_f32_fp8_e32 v[66:67], v70
	v_cvt_pk_f32_fp8_sdwa v[68:69], v70 src0_sel:WORD_1
	v_cvt_pk_f32_fp8_e32 v[70:71], v72
	v_cvt_pk_f32_fp8_sdwa v[72:73], v72 src0_sel:WORD_1
	v_pk_mul_f32 v[70:71], v[80:81], v[70:71] op_sel_hi:[0,1]
	v_pk_fma_f32 v[66:67], v[78:79], v[66:67], v[70:71] op_sel_hi:[0,1,1]
	v_pk_add_f32 v[104:105], v[66:67], v[74:75]
	v_pk_mul_f32 v[66:67], v[80:81], v[72:73] op_sel_hi:[0,1]
	v_pk_fma_f32 v[66:67], v[78:79], v[68:69], v[66:67] op_sel_hi:[0,1,1]
	v_cvt_pk_f32_fp8_e32 v[68:69], v77
	v_pk_add_f32 v[106:107], v[66:67], v[64:65]
	v_cvt_pk_f32_fp8_e32 v[64:65], v76
	v_cvt_pk_f32_fp8_sdwa v[70:71], v77 src0_sel:WORD_1
	v_cvt_pk_f32_fp8_sdwa v[66:67], v76 src0_sel:WORD_1
	v_pk_mul_f32 v[68:69], v[80:81], v[68:69] op_sel_hi:[0,1]
	v_lshlrev_b32_e32 v72, 16, v62
	v_and_b32_e32 v73, 0xffff0000, v62
	v_pk_fma_f32 v[64:65], v[78:79], v[64:65], v[68:69] op_sel_hi:[0,1,1]
	v_pk_add_f32 v[74:75], v[64:65], v[72:73]
	v_pk_mul_f32 v[64:65], v[80:81], v[70:71] op_sel_hi:[0,1]
	v_lshlrev_b32_e32 v62, 16, v63
	v_and_b32_e32 v63, 0xffff0000, v63
	v_pk_fma_f32 v[64:65], v[78:79], v[66:67], v[64:65] op_sel_hi:[0,1,1]
	v_cvt_pk_f32_fp8_e32 v[66:67], v100
	v_pk_add_f32 v[76:77], v[64:65], v[62:63]
	v_cvt_pk_f32_fp8_e32 v[62:63], v79
	v_cvt_pk_f32_fp8_sdwa v[68:69], v100 src0_sel:WORD_1
	v_cvt_pk_f32_fp8_sdwa v[64:65], v79 src0_sel:WORD_1
	v_pk_mul_f32 v[66:67], v[80:81], v[66:67] op_sel_hi:[0,1]
	v_lshlrev_b32_e32 v70, 16, v60
	v_and_b32_e32 v71, 0xffff0000, v60
	v_pk_fma_f32 v[62:63], v[78:79], v[62:63], v[66:67] op_sel_hi:[0,1,1]
	v_pk_add_f32 v[70:71], v[62:63], v[70:71]
	v_pk_mul_f32 v[62:63], v[80:81], v[68:69] op_sel_hi:[0,1]
	v_lshlrev_b32_e32 v60, 16, v61
	v_and_b32_e32 v61, 0xffff0000, v61
	v_pk_fma_f32 v[62:63], v[78:79], v[64:65], v[62:63] op_sel_hi:[0,1,1]
	v_cvt_pk_f32_fp8_e32 v[64:65], v102
	v_pk_add_f32 v[72:73], v[62:63], v[60:61]
	v_cvt_pk_f32_fp8_e32 v[60:61], v101
	v_cvt_pk_f32_fp8_sdwa v[68:69], v102 src0_sel:WORD_1
	v_cvt_pk_f32_fp8_sdwa v[62:63], v101 src0_sel:WORD_1
	v_pk_mul_f32 v[64:65], v[80:81], v[64:65] op_sel_hi:[0,1]
	v_lshlrev_b32_e32 v66, 16, v58
	v_and_b32_e32 v67, 0xffff0000, v58
	v_pk_fma_f32 v[60:61], v[78:79], v[60:61], v[64:65] op_sel_hi:[0,1,1]
	v_pk_add_f32 v[66:67], v[60:61], v[66:67]
	v_pk_mul_f32 v[60:61], v[80:81], v[68:69] op_sel_hi:[0,1]
	v_lshlrev_b32_e32 v58, 16, v59
	v_and_b32_e32 v59, 0xffff0000, v59
	v_pk_fma_f32 v[60:61], v[78:79], v[62:63], v[60:61] op_sel_hi:[0,1,1]
	v_cvt_pk_f32_fp8_e32 v[62:63], v108
	v_pk_add_f32 v[68:69], v[60:61], v[58:59]
	v_cvt_pk_f32_fp8_e32 v[58:59], v103
	v_cvt_pk_f32_fp8_sdwa v[64:65], v108 src0_sel:WORD_1
	v_cvt_pk_f32_fp8_sdwa v[60:61], v103 src0_sel:WORD_1
	v_pk_mul_f32 v[62:63], v[80:81], v[62:63] op_sel_hi:[0,1]
	v_lshlrev_b32_e32 v100, 16, v48
	v_and_b32_e32 v101, 0xffff0000, v48
	v_pk_fma_f32 v[58:59], v[78:79], v[58:59], v[62:63] op_sel_hi:[0,1,1]
	v_pk_add_f32 v[62:63], v[58:59], v[100:101]
	v_pk_mul_f32 v[58:59], v[80:81], v[64:65] op_sel_hi:[0,1]
	v_lshlrev_b32_e32 v48, 16, v49
	v_and_b32_e32 v49, 0xffff0000, v49
	v_pk_fma_f32 v[58:59], v[78:79], v[60:61], v[58:59] op_sel_hi:[0,1,1]
	v_pk_add_f32 v[64:65], v[58:59], v[48:49]
	v_cvt_pk_f32_fp8_e32 v[58:59], v110
	v_cvt_pk_f32_fp8_e32 v[48:49], v109
	v_cvt_pk_f32_fp8_sdwa v[100:101], v110 src0_sel:WORD_1
	v_cvt_pk_f32_fp8_sdwa v[60:61], v109 src0_sel:WORD_1
	v_pk_mul_f32 v[58:59], v[80:81], v[58:59] op_sel_hi:[0,1]
	v_lshlrev_b32_e32 v102, 16, v46
	v_and_b32_e32 v103, 0xffff0000, v46
	v_pk_fma_f32 v[48:49], v[78:79], v[48:49], v[58:59] op_sel_hi:[0,1,1]
	v_pk_add_f32 v[58:59], v[48:49], v[102:103]
	v_pk_mul_f32 v[48:49], v[80:81], v[100:101] op_sel_hi:[0,1]
	v_lshlrev_b32_e32 v46, 16, v47
	v_and_b32_e32 v47, 0xffff0000, v47
	v_pk_fma_f32 v[48:49], v[78:79], v[60:61], v[48:49] op_sel_hi:[0,1,1]
	v_cvt_pk_f32_fp8_e32 v[100:101], v112
	v_pk_add_f32 v[60:61], v[48:49], v[46:47]
	v_cvt_pk_f32_fp8_e32 v[46:47], v111
	v_cvt_pk_f32_fp8_sdwa v[102:103], v112 src0_sel:WORD_1
	v_cvt_pk_f32_fp8_sdwa v[48:49], v111 src0_sel:WORD_1
	v_pk_mul_f32 v[100:101], v[80:81], v[100:101] op_sel_hi:[0,1]
	v_pk_fma_f32 v[46:47], v[78:79], v[46:47], v[100:101] op_sel_hi:[0,1,1]
	v_pk_mul_f32 v[100:101], v[80:81], v[102:103] op_sel_hi:[0,1]
	v_lshlrev_b32_e32 v108, 16, v42
	v_and_b32_e32 v109, 0xffff0000, v42
	v_lshlrev_b32_e32 v42, 16, v43
	v_and_b32_e32 v43, 0xffff0000, v43
	v_pk_fma_f32 v[48:49], v[78:79], v[48:49], v[100:101] op_sel_hi:[0,1,1]
	v_cvt_pk_f32_fp8_e32 v[102:103], v114
	v_pk_add_f32 v[46:47], v[46:47], v[108:109]
; #define GAS __attribute__((address_space(1)))
; __device__ __forceinline__ unsigned pk2(float lo, float hi) { f32x2_m v = {lo, hi}; bf16x2_m b = __builtin_convertvector(v, bf16x2_m); return __builtin_bit_cast(unsigned, b); }
; template <int MODE, bool W8 = false>
; __device__ __forceinline__ void norm_rows(const Ctx& C, const void* src, bf16* xdst, const unsigned char* YS8, const int* srow, const float* gate, const float* gain, bf16* XN, float* outf, unsigned char* XN8 = nullptr) {
;     ...
;                 for (int j = 0; j < 8; ++j) { const unsigned a = ya[q][j], b = yb[q][j];
;                     const f32x2_m a01 = __builtin_amdgcn_cvt_pk_f32_fp8((int)a, false), a23 = __builtin_amdgcn_cvt_pk_f32_fp8((int)a, true), b01 = __builtin_amdgcn_cvt_pk_f32_fp8((int)b, false), b23 = __builtin_amdgcn_cvt_pk_f32_fp8((int)b, true);
;                     v[q][j].x += h0[q] * a01.x + h1[q] * b01.x; v[q][j].y += h0[q] * a01.y + h1[q] * b01.y; v[q][j].z += h0[q] * a23.x + h1[q] * b23.x; v[q][j].w += h0[q] * a23.y + h1[q] * b23.y; } }
;             float ss = 0.f;
; #pragma unroll
;             for (int j = 0; j < 8; ++j) ss += (v[q][j].x * v[q][j].x + v[q][j].y * v[q][j].y) + (v[q][j].z * v[q][j].z + v[q][j].w * v[q][j].w);
;             const float rstd = 1.0f / sqrtf(wave_sum(ss) * (1.0f / DM) + RMS_EPS);
;             if (MODE == 1) { GAS v2u* xo = (GAS v2u*)(xdst + (size_t)m * DM) + C.lane;
; #pragma unroll
;                 for (int j = 0; j < 8; ++j) { v2u w; w.x = pk2(v[q][j].x, v[q][j].y); w.y = pk2(v[q][j].z, v[q][j].w); xo[64 * j] = w; } }
	v_pk_add_f32 v[48:49], v[48:49], v[42:43]
	v_cvt_pk_f32_fp8_e32 v[42:43], v113
	v_cvt_pk_f32_fp8_sdwa v[108:109], v114 src0_sel:WORD_1
	v_cvt_pk_f32_fp8_sdwa v[100:101], v113 src0_sel:WORD_1
	v_pk_mul_f32 v[102:103], v[80:81], v[102:103] op_sel_hi:[0,1]
	v_pk_fma_f32 v[42:43], v[78:79], v[42:43], v[102:103] op_sel_hi:[0,1,1]
	v_pk_mul_f32 v[102:103], v[80:81], v[108:109] op_sel_hi:[0,1]
	v_lshlrev_b32_e32 v110, 16, v44
	v_and_b32_e32 v111, 0xffff0000, v44
	v_lshlrev_b32_e32 v44, 16, v45
	v_and_b32_e32 v45, 0xffff0000, v45
	v_pk_fma_f32 v[78:79], v[78:79], v[100:101], v[102:103] op_sel_hi:[0,1,1]
	v_mov_b32_e32 v100, v105
	v_mov_b32_e32 v101, v75
	v_pk_add_f32 v[44:45], v[78:79], v[44:45]
	v_mov_b32_e32 v78, v104
	v_mov_b32_e32 v79, v74
	v_pk_mul_f32 v[100:101], v[100:101], v[100:101]
	v_mov_b32_e32 v102, v107
	v_mov_b32_e32 v103, v77
	v_pk_fma_f32 v[78:79], v[78:79], v[78:79], v[100:101]
	v_mov_b32_e32 v100, v106
	v_mov_b32_e32 v101, v76
	v_pk_mul_f32 v[102:103], v[102:103], v[102:103]
	v_mul_f32_e32 v80, v67, v67
	v_pk_fma_f32 v[100:101], v[100:101], v[100:101], v[102:103]
	v_mov_b32_e32 v102, v71
	v_mov_b32_e32 v103, v73
	v_pk_add_f32 v[78:79], v[78:79], v[100:101]
	v_mov_b32_e32 v100, v70
	v_mov_b32_e32 v101, v72
	v_pk_mul_f32 v[102:103], v[102:103], v[102:103]
	v_pk_add_f32 v[42:43], v[42:43], v[110:111]
	v_pk_fma_f32 v[100:101], v[100:101], v[100:101], v[102:103]
	v_pk_fma_f32 v[102:103], v[66:67], v[66:67], v[80:81] op_sel_hi:[1,1,0]
	v_mul_f32_e32 v80, v69, v69
	v_pk_add_f32 v[78:79], v[78:79], v[78:79] op_sel:[0,1] op_sel_hi:[1,0]
	v_pk_add_f32 v[100:101], v[100:101], v[100:101] op_sel:[0,1] op_sel_hi:[1,0]
	v_pk_fma_f32 v[108:109], v[68:69], v[68:69], v[80:81] op_sel_hi:[1,1,0]
	v_pk_mul_f32 v[110:111], v[62:63], v[62:63]
	v_pk_mul_f32 v[112:113], v[64:65], v[64:65]
	v_mov_b32_e32 v79, v110
	v_mov_b32_e32 v101, v111
	v_mov_b32_e32 v103, v112
	v_mov_b32_e32 v109, v113
	v_pk_add_f32 v[78:79], v[78:79], v[100:101]
	v_pk_add_f32 v[100:101], v[102:103], v[108:109]
	v_mov_b32_e32 v102, v59
	v_mov_b32_e32 v103, v61
	v_pk_add_f32 v[78:79], v[78:79], v[100:101]
	v_mov_b32_e32 v100, v58
	v_mov_b32_e32 v101, v60
	v_pk_mul_f32 v[102:103], v[102:103], v[102:103]
	v_mul_f32_e32 v80, v47, v47
	v_pk_fma_f32 v[100:101], v[100:101], v[100:101], v[102:103]
	v_pk_fma_f32 v[102:103], v[46:47], v[46:47], v[80:81] op_sel_hi:[1,1,0]
	v_mul_f32_e32 v80, v49, v49
	v_pk_add_f32 v[78:79], v[78:79], v[78:79] op_sel:[0,1] op_sel_hi:[1,0]
	v_pk_add_f32 v[100:101], v[100:101], v[100:101] op_sel:[0,1] op_sel_hi:[1,0]
	v_pk_fma_f32 v[108:109], v[48:49], v[48:49], v[80:81] op_sel_hi:[1,1,0]
	v_pk_mul_f32 v[110:111], v[42:43], v[42:43]
	v_pk_mul_f32 v[112:113], v[44:45], v[44:45]
	v_mov_b32_e32 v79, v110
	v_mov_b32_e32 v101, v111
	v_mov_b32_e32 v103, v112
	v_mov_b32_e32 v109, v113
	v_pk_add_f32 v[78:79], v[78:79], v[100:101]
	v_pk_add_f32 v[100:101], v[102:103], v[108:109]
	s_nop 0
	v_pk_add_f32 v[78:79], v[78:79], v[100:101]
	s_nop 0
	v_add_f32_e32 v78, v78, v79
	ds_bpermute_b32 v79, v3, v78
	s_waitcnt lgkmcnt(0)
	v_add_f32_e32 v78, v78, v79
	ds_bpermute_b32 v79, v57, v78
	s_waitcnt lgkmcnt(0)
	v_add_f32_e32 v78, v78, v79
	ds_bpermute_b32 v79, v81, v78
	s_waitcnt lgkmcnt(0)
	v_add_f32_e32 v78, v78, v79
	ds_bpermute_b32 v79, v82, v78
	s_waitcnt lgkmcnt(0)
	v_add_f32_e32 v78, v78, v79
	ds_bpermute_b32 v79, v83, v78
	s_waitcnt lgkmcnt(0)
	v_add_f32_e32 v78, v78, v79
	ds_bpermute_b32 v79, v84, v78
	s_waitcnt lgkmcnt(0)
	v_add_f32_e32 v78, v78, v79
	v_fmamk_f32 v78, v78, 0x3a000000, v212
	v_cmp_gt_f32_e32 vcc, s12, v78
	v_mul_f32_e32 v79, 0x4f800000, v78
	s_nop 0
	v_cndmask_b32_e32 v78, v78, v79, vcc
	v_sqrt_f32_e32 v79, v78
	s_nop 0
	v_add_u32_e32 v80, -1, v79
	v_fma_f32 v100, -v80, v79, v78
	v_cmp_ge_f32_e64 s[2:3], 0, v100
	v_add_u32_e32 v100, 1, v79
	s_nop 0
	v_cndmask_b32_e64 v80, v79, v80, s[2:3]
	v_fma_f32 v79, -v100, v79, v78
	v_cmp_lt_f32_e64 s[2:3], 0, v79
	s_nop 1
	v_cndmask_b32_e64 v79, v80, v100, s[2:3]
	v_mul_f32_e32 v80, 0x37800000, v79
	v_cndmask_b32_e32 v79, v79, v80, vcc
	v_cmp_class_f32_e32 vcc, v78, v211
	s_nop 1
	v_cndmask_b32_e32 v80, v79, v78, vcc
	v_cvt_pk_bf16_f32 v78, v104, v105
	v_cvt_pk_bf16_f32 v79, v106, v107
	global_store_dwordx2 v[50:51], v[78:79], off
	s_nop 1
	v_cvt_pk_bf16_f32 v78, v74, v75
	v_cvt_pk_bf16_f32 v79, v76, v77
	global_store_dwordx2 v[50:51], v[78:79], off offset:512
	s_nop 1
	v_cvt_pk_bf16_f32 v78, v70, v71
	v_cvt_pk_bf16_f32 v79, v72, v73
	global_store_dwordx2 v[50:51], v[78:79], off offset:1024
	s_nop 1
	v_cvt_pk_bf16_f32 v78, v66, v67
	v_cvt_pk_bf16_f32 v79, v68, v69
	global_store_dwordx2 v[50:51], v[78:79], off offset:1536
	s_nop 1
	v_cvt_pk_bf16_f32 v78, v62, v63
	v_cvt_pk_bf16_f32 v79, v64, v65
	global_store_dwordx2 v[50:51], v[78:79], off offset:2048
	s_nop 1
	v_cvt_pk_bf16_f32 v78, v58, v59
	v_cvt_pk_bf16_f32 v79, v60, v61
	global_store_dwordx2 v[50:51], v[78:79], off offset:2560
	s_nop 1
	v_cvt_pk_bf16_f32 v78, v46, v47
	v_cvt_pk_bf16_f32 v79, v48, v49
	global_store_dwordx2 v[50:51], v[78:79], off offset:3072
	s_nop 1
	v_cvt_pk_bf16_f32 v78, v42, v43
	v_cvt_pk_bf16_f32 v79, v44, v45
	global_store_dwordx2 v[50:51], v[78:79], off offset:3584
	s_nop 1
	v_div_scale_f32 v50, s[2:3], v80, v80, 1.0
	v_rcp_f32_e32 v51, v50
	s_nop 0
	v_fma_f32 v78, -v50, v51, 1.0
	v_fmac_f32_e32 v51, v78, v51
	v_div_scale_f32 v78, vcc, 1.0, v80, 1.0
	v_mul_f32_e32 v79, v78, v51
	v_fma_f32 v100, -v50, v79, v78
	v_fmac_f32_e32 v79, v100, v51
	v_fma_f32 v50, -v50, v79, v78
	v_div_fmas_f32 v50, v50, v51, v79
	v_div_fixup_f32 v50, v50, v80, 1.0
	v_pk_mul_f32 v[78:79], v[104:105], v[50:51] op_sel_hi:[1,0]
	v_pk_mul_f32 v[104:105], v[106:107], v[50:51] op_sel_hi:[1,0]
; #define GAS __attribute__((address_space(1)))
; __device__ __forceinline__ unsigned pk2(float lo, float hi) { f32x2_m v = {lo, hi}; bf16x2_m b = __builtin_convertvector(v, bf16x2_m); return __builtin_bit_cast(unsigned, b); }
; template <int MODE, bool W8 = false>
; __device__ __forceinline__ void norm_rows(const Ctx& C, const void* src, bf16* xdst, const unsigned char* YS8, const int* srow, const float* gate, const float* gain, bf16* XN, float* outf, unsigned char* XN8 = nullptr) {
;     ...
;             const GAS f32x4* gg = (const GAS f32x4*)gain + C.lane;
;             if (MODE <= 1) { GAS v2u* o = (GAS v2u*)(XN + (size_t)m * DM) + C.lane;
; #pragma unroll
;                 for (int j = 0; j < 8; ++j) { const f32x4 g = gg[64 * j]; const f32x4 y = v[q][j] * rstd * g; v2u w; w.x = pk2(y.x, y.y); w.y = pk2(y.z, y.w); o[64 * j] = w;
;                     if constexpr (W8) ((GAS unsigned*)(XN8 + (size_t)m * DM) + C.lane)[64 * j] = pk4_fp8m(y.x * SXN, y.y * SXN, y.z * SXN, y.w * SXN); } }
	v_add_co_u32_e32 v52, vcc, s16, v52
	v_pk_mul_f32 v[102:103], v[162:163], v[104:105]
	v_pk_mul_f32 v[78:79], v[160:161], v[78:79]
	v_cvt_pk_bf16_f32 v101, v102, v103
	v_cvt_pk_bf16_f32 v100, v78, v79
	v_addc_co_u32_e32 v53, vcc, 0, v53, vcc
	v_mul_f32_e32 v51, 0x42000000, v78
	v_mul_f32_e32 v78, 0x42000000, v79
	global_store_dwordx2 v[52:53], v[100:101], off
	s_nop 1
	v_med3_f32 v51, v51, s33, v214
	v_med3_f32 v78, v78, s33, v214
	v_mov_b32_e32 v100, v2
	v_cvt_pk_fp8_f32 v100, v51, v78
	v_mul_f32_e32 v79, 0x42000000, v102
	v_mul_f32_e32 v80, 0x42000000, v103
	v_med3_f32 v79, v79, s33, v214
	v_med3_f32 v80, v80, s33, v214
	v_cvt_pk_fp8_f32 v100, v79, v80 op_sel:[0,0,1]
	v_lshl_add_u64 v[78:79], s[4:5], 0, v[18:19]
	v_add_co_u32_e32 v78, vcc, s17, v78
	v_pk_mul_f32 v[74:75], v[74:75], v[50:51] op_sel_hi:[1,0]
	s_nop 0
	v_addc_co_u32_e32 v79, vcc, 0, v79, vcc
	global_store_dword v[78:79], v100, off
	s_nop 1
	v_pk_mul_f32 v[76:77], v[76:77], v[50:51] op_sel_hi:[1,0]
	v_lshl_add_u64 v[18:19], v[18:19], 0, s[18:19]
	v_pk_mul_f32 v[74:75], v[164:165], v[74:75]
	v_pk_mul_f32 v[76:77], v[166:167], v[76:77]
	v_cvt_pk_bf16_f32 v100, v74, v75
	v_mul_f32_e32 v51, 0x42000000, v74
	v_mul_f32_e32 v74, 0x42000000, v75
	v_cvt_pk_bf16_f32 v101, v76, v77
	v_mul_f32_e32 v75, 0x42000000, v76
	v_mul_f32_e32 v76, 0x42000000, v77
	v_med3_f32 v51, v51, s33, v214
	v_med3_f32 v74, v74, s33, v214
	v_mov_b32_e32 v77, v2
	v_cvt_pk_fp8_f32 v77, v51, v74
	v_med3_f32 v75, v75, s33, v214
	v_med3_f32 v76, v76, s33, v214
	global_store_dwordx2 v[52:53], v[100:101], off offset:512
	s_nop 1
	v_cvt_pk_fp8_f32 v77, v75, v76 op_sel:[0,0,1]
	v_pk_mul_f32 v[70:71], v[70:71], v[50:51] op_sel_hi:[1,0]
	v_pk_mul_f32 v[72:73], v[72:73], v[50:51] op_sel_hi:[1,0]
	global_store_dword v[78:79], v77, off offset:256
	s_nop 1
	v_pk_mul_f32 v[70:71], v[70:71], v[168:169]
	v_pk_mul_f32 v[72:73], v[72:73], v[170:171]
	v_cvt_pk_bf16_f32 v74, v70, v71
	v_mul_f32_e32 v51, 0x42000000, v70
	v_mul_f32_e32 v70, 0x42000000, v71
	v_cvt_pk_bf16_f32 v75, v72, v73
	v_mul_f32_e32 v71, 0x42000000, v72
	v_mul_f32_e32 v72, 0x42000000, v73
	v_med3_f32 v51, v51, s33, v214
	v_med3_f32 v70, v70, s33, v214
	v_mov_b32_e32 v73, v2
	v_cvt_pk_fp8_f32 v73, v51, v70
	v_med3_f32 v71, v71, s33, v214
	v_med3_f32 v72, v72, s33, v214
	global_store_dwordx2 v[52:53], v[74:75], off offset:1024
	s_nop 1
	v_cvt_pk_fp8_f32 v73, v71, v72 op_sel:[0,0,1]
	v_pk_mul_f32 v[66:67], v[66:67], v[50:51] op_sel_hi:[1,0]
	v_pk_mul_f32 v[68:69], v[68:69], v[50:51] op_sel_hi:[1,0]
	global_store_dword v[78:79], v73, off offset:512
	s_nop 1
	v_pk_mul_f32 v[66:67], v[66:67], v[172:173]
	v_pk_mul_f32 v[68:69], v[68:69], v[174:175]
	v_cvt_pk_bf16_f32 v70, v66, v67
	v_mul_f32_e32 v51, 0x42000000, v66
	v_mul_f32_e32 v66, 0x42000000, v67
	v_cvt_pk_bf16_f32 v71, v68, v69
	v_mul_f32_e32 v67, 0x42000000, v68
	v_mul_f32_e32 v68, 0x42000000, v69
	v_med3_f32 v51, v51, s33, v214
	v_med3_f32 v66, v66, s33, v214
	v_mov_b32_e32 v69, v2
	v_cvt_pk_fp8_f32 v69, v51, v66
	v_med3_f32 v67, v67, s33, v214
	v_med3_f32 v68, v68, s33, v214
	global_store_dwordx2 v[52:53], v[70:71], off offset:1536
	s_nop 1
	v_cvt_pk_fp8_f32 v69, v67, v68 op_sel:[0,0,1]
	v_pk_mul_f32 v[62:63], v[62:63], v[50:51] op_sel_hi:[1,0]
	v_pk_mul_f32 v[64:65], v[64:65], v[50:51] op_sel_hi:[1,0]
	global_store_dword v[78:79], v69, off offset:768
	s_nop 1
	v_pk_mul_f32 v[62:63], v[62:63], v[176:177]
	v_pk_mul_f32 v[64:65], v[64:65], v[178:179]
	v_cvt_pk_bf16_f32 v66, v62, v63
	v_mul_f32_e32 v51, 0x42000000, v62
	v_mul_f32_e32 v62, 0x42000000, v63
	v_cvt_pk_bf16_f32 v67, v64, v65
	v_mul_f32_e32 v63, 0x42000000, v64
	v_mul_f32_e32 v64, 0x42000000, v65
	v_med3_f32 v51, v51, s33, v214
	v_med3_f32 v62, v62, s33, v214
	v_mov_b32_e32 v65, v2
	v_cvt_pk_fp8_f32 v65, v51, v62
	v_med3_f32 v63, v63, s33, v214
	v_med3_f32 v64, v64, s33, v214
	global_store_dwordx2 v[52:53], v[66:67], off offset:2048
	s_nop 1
	v_cvt_pk_fp8_f32 v65, v63, v64 op_sel:[0,0,1]
	v_pk_mul_f32 v[58:59], v[58:59], v[50:51] op_sel_hi:[1,0]
	v_pk_mul_f32 v[60:61], v[60:61], v[50:51] op_sel_hi:[1,0]
	v_lshlrev_b32_e32 v66, 16, v22
	global_store_dword v[78:79], v65, off offset:1024
	s_nop 1
	v_and_b32_e32 v67, 0xffff0000, v22
	v_lshlrev_b32_e32 v22, 16, v23
	v_and_b32_e32 v23, 0xffff0000, v23
	v_lshlrev_b32_e32 v68, 16, v24
	v_and_b32_e32 v69, 0xffff0000, v24
	v_lshlrev_b32_e32 v24, 16, v25
	v_and_b32_e32 v25, 0xffff0000, v25
	v_pk_mul_f32 v[58:59], v[58:59], v[180:181]
	v_pk_mul_f32 v[60:61], v[60:61], v[182:183]
	v_cvt_pk_bf16_f32 v62, v58, v59
	v_mul_f32_e32 v51, 0x42000000, v58
	v_mul_f32_e32 v58, 0x42000000, v59
	v_cvt_pk_bf16_f32 v63, v60, v61
	v_mul_f32_e32 v59, 0x42000000, v60
	v_mul_f32_e32 v60, 0x42000000, v61
	v_med3_f32 v51, v51, s33, v214
	v_med3_f32 v58, v58, s33, v214
	v_mov_b32_e32 v61, v2
	v_cvt_pk_fp8_f32 v61, v51, v58
	v_med3_f32 v59, v59, s33, v214
	v_med3_f32 v60, v60, s33, v214
	global_store_dwordx2 v[52:53], v[62:63], off offset:2560
	s_nop 1
	v_cvt_pk_fp8_f32 v61, v59, v60 op_sel:[0,0,1]
	v_pk_mul_f32 v[46:47], v[46:47], v[50:51] op_sel_hi:[1,0]
	v_pk_mul_f32 v[48:49], v[48:49], v[50:51] op_sel_hi:[1,0]
	v_mov_b32_e32 v51, v2
	global_store_dword v[78:79], v61, off offset:1280
	s_nop 1
	v_pk_mul_f32 v[46:47], v[46:47], v[184:185]
	s_nop 0
	v_cvt_pk_bf16_f32 v58, v46, v47
	v_mul_f32_e32 v46, 0x42000000, v46
	v_mul_f32_e32 v47, 0x42000000, v47
	v_med3_f32 v46, v46, s33, v214
	v_med3_f32 v47, v47, s33, v214
	v_cvt_pk_fp8_f32 v51, v46, v47
	v_pk_mul_f32 v[48:49], v[48:49], v[186:187]
	v_lshlrev_b32_e32 v60, 16, v30
	v_cvt_pk_bf16_f32 v59, v48, v49
	v_mul_f32_e32 v48, 0x42000000, v48
	v_mul_f32_e32 v49, 0x42000000, v49
	v_med3_f32 v48, v48, s33, v214
	v_med3_f32 v49, v49, s33, v214
	v_cvt_pk_fp8_f32 v51, v48, v49 op_sel:[0,0,1]
	global_store_dwordx2 v[52:53], v[58:59], off offset:3072
	s_nop 1
	v_lshlrev_b32_e32 v58, 16, v32
	v_and_b32_e32 v59, 0xffff0000, v32
	global_store_dword v[78:79], v51, off offset:1536
	s_nop 1
	v_pk_mul_f32 v[42:43], v[42:43], v[50:51] op_sel_hi:[1,0]
	v_pk_mul_f32 v[44:45], v[44:45], v[50:51] op_sel_hi:[1,0]
	v_lshlrev_b32_e32 v50, 16, v40
	v_and_b32_e32 v51, 0xffff0000, v40
	v_lshlrev_b32_e32 v40, 16, v41
	v_and_b32_e32 v41, 0xffff0000, v41
	v_lshlrev_b32_e32 v32, 16, v33
	v_and_b32_e32 v33, 0xffff0000, v33
	v_and_b32_e32 v61, 0xffff0000, v30
	v_lshlrev_b32_e32 v30, 16, v31
	v_and_b32_e32 v31, 0xffff0000, v31
	v_pk_mul_f32 v[44:45], v[44:45], v[190:191]
	v_pk_mul_f32 v[42:43], v[42:43], v[188:189]
	v_cvt_pk_bf16_f32 v47, v44, v45
	v_cvt_pk_bf16_f32 v46, v42, v43
	v_mul_f32_e32 v42, 0x42000000, v42
	v_mul_f32_e32 v43, 0x42000000, v43
	global_store_dwordx2 v[52:53], v[46:47], off offset:3584
	s_nop 1
	v_med3_f32 v42, v42, s33, v214
	v_med3_f32 v43, v43, s33, v214
	v_mov_b32_e32 v46, v2
	v_cvt_pk_fp8_f32 v46, v42, v43
	v_mul_f32_e32 v44, 0x42000000, v44
	v_mul_f32_e32 v45, 0x42000000, v45
	v_med3_f32 v44, v44, s33, v214
	v_med3_f32 v45, v45, s33, v214
	v_cvt_pk_fp8_f32 v46, v44, v45 op_sel:[0,0,1]
	s_waitcnt vmcnt(23)
; template <int MODE, bool W8 = false>
; __device__ __forceinline__ void norm_rows(const Ctx& C, const void* src, bf16* xdst, const unsigned char* YS8, const int* srow, const float* gate, const float* gain, bf16* XN, float* outf, unsigned char* XN8 = nullptr) {
;     ...
;                 for (int j = 0; j < 8; ++j) { const unsigned a = ya[q][j], b = yb[q][j];
;                     const f32x2_m a01 = __builtin_amdgcn_cvt_pk_f32_fp8((int)a, false), a23 = __builtin_amdgcn_cvt_pk_f32_fp8((int)a, true), b01 = __builtin_amdgcn_cvt_pk_f32_fp8((int)b, false), b23 = __builtin_amdgcn_cvt_pk_f32_fp8((int)b, true);
;                     v[q][j].x += h0[q] * a01.x + h1[q] * b01.x; v[q][j].y += h0[q] * a01.y + h1[q] * b01.y; v[q][j].z += h0[q] * a23.x + h1[q] * b23.x; v[q][j].w += h0[q] * a23.y + h1[q] * b23.y; } }
;             float ss = 0.f;
; #pragma unroll
;             for (int j = 0; j < 8; ++j) ss += (v[q][j].x * v[q][j].x + v[q][j].y * v[q][j].y) + (v[q][j].z * v[q][j].z + v[q][j].w * v[q][j].w);
;             const float rstd = 1.0f / sqrtf(wave_sum(ss) * (1.0f / DM) + RMS_EPS);
	v_cvt_pk_f32_fp8_e32 v[42:43], v99
	v_cvt_pk_f32_fp8_sdwa v[48:49], v98 src0_sel:WORD_1
	v_cvt_pk_f32_fp8_sdwa v[44:45], v99 src0_sel:WORD_1
	global_store_dword v[78:79], v46, off offset:1792
	s_nop 1
	v_cvt_pk_f32_fp8_e32 v[46:47], v98
	v_pk_mul_f32 v[46:47], v[56:57], v[46:47] op_sel_hi:[0,1]
	v_pk_fma_f32 v[42:43], v[54:55], v[42:43], v[46:47] op_sel_hi:[0,1,1]
	v_pk_add_f32 v[62:63], v[42:43], v[50:51]
	v_pk_mul_f32 v[42:43], v[56:57], v[48:49] op_sel_hi:[0,1]
	v_pk_fma_f32 v[42:43], v[54:55], v[44:45], v[42:43] op_sel_hi:[0,1,1]
	v_cvt_pk_f32_fp8_e32 v[44:45], v96
	v_pk_add_f32 v[64:65], v[42:43], v[40:41]
	v_cvt_pk_f32_fp8_e32 v[40:41], v97
	v_cvt_pk_f32_fp8_sdwa v[46:47], v96 src0_sel:WORD_1
	v_cvt_pk_f32_fp8_sdwa v[42:43], v97 src0_sel:WORD_1
	v_pk_mul_f32 v[44:45], v[56:57], v[44:45] op_sel_hi:[0,1]
	v_lshlrev_b32_e32 v48, 16, v38
	v_and_b32_e32 v49, 0xffff0000, v38
	v_pk_fma_f32 v[40:41], v[54:55], v[40:41], v[44:45] op_sel_hi:[0,1,1]
	v_pk_add_f32 v[50:51], v[40:41], v[48:49]
	v_pk_mul_f32 v[40:41], v[56:57], v[46:47] op_sel_hi:[0,1]
	v_lshlrev_b32_e32 v38, 16, v39
	v_and_b32_e32 v39, 0xffff0000, v39
	v_pk_fma_f32 v[40:41], v[54:55], v[42:43], v[40:41] op_sel_hi:[0,1,1]
	v_cvt_pk_f32_fp8_e32 v[42:43], v94
	v_pk_add_f32 v[52:53], v[40:41], v[38:39]
	v_cvt_pk_f32_fp8_e32 v[38:39], v95
	v_cvt_pk_f32_fp8_sdwa v[44:45], v94 src0_sel:WORD_1
	v_cvt_pk_f32_fp8_sdwa v[40:41], v95 src0_sel:WORD_1
	v_pk_mul_f32 v[42:43], v[56:57], v[42:43] op_sel_hi:[0,1]
	v_lshlrev_b32_e32 v46, 16, v36
	v_and_b32_e32 v47, 0xffff0000, v36
	v_pk_fma_f32 v[38:39], v[54:55], v[38:39], v[42:43] op_sel_hi:[0,1,1]
	v_pk_add_f32 v[46:47], v[38:39], v[46:47]
	v_pk_mul_f32 v[38:39], v[56:57], v[44:45] op_sel_hi:[0,1]
	v_lshlrev_b32_e32 v36, 16, v37
	v_and_b32_e32 v37, 0xffff0000, v37
	v_pk_fma_f32 v[38:39], v[54:55], v[40:41], v[38:39] op_sel_hi:[0,1,1]
	v_cvt_pk_f32_fp8_e32 v[40:41], v92
	v_pk_add_f32 v[48:49], v[38:39], v[36:37]
	v_cvt_pk_f32_fp8_e32 v[36:37], v93
	v_cvt_pk_f32_fp8_sdwa v[44:45], v92 src0_sel:WORD_1
	v_cvt_pk_f32_fp8_sdwa v[38:39], v93 src0_sel:WORD_1
	v_pk_mul_f32 v[40:41], v[56:57], v[40:41] op_sel_hi:[0,1]
	v_lshlrev_b32_e32 v42, 16, v34
	v_and_b32_e32 v43, 0xffff0000, v34
	v_pk_fma_f32 v[36:37], v[54:55], v[36:37], v[40:41] op_sel_hi:[0,1,1]
	v_pk_add_f32 v[42:43], v[36:37], v[42:43]
	v_pk_mul_f32 v[36:37], v[56:57], v[44:45] op_sel_hi:[0,1]
	v_lshlrev_b32_e32 v34, 16, v35
	v_and_b32_e32 v35, 0xffff0000, v35
	v_pk_fma_f32 v[36:37], v[54:55], v[38:39], v[36:37] op_sel_hi:[0,1,1]
	v_cvt_pk_f32_fp8_e32 v[38:39], v90
	v_pk_add_f32 v[44:45], v[36:37], v[34:35]
	v_cvt_pk_f32_fp8_e32 v[34:35], v91
	v_cvt_pk_f32_fp8_sdwa v[40:41], v90 src0_sel:WORD_1
	v_cvt_pk_f32_fp8_sdwa v[36:37], v91 src0_sel:WORD_1
	v_pk_mul_f32 v[38:39], v[56:57], v[38:39] op_sel_hi:[0,1]
	v_pk_fma_f32 v[34:35], v[54:55], v[34:35], v[38:39] op_sel_hi:[0,1,1]
	v_pk_add_f32 v[38:39], v[34:35], v[58:59]
	v_pk_mul_f32 v[34:35], v[56:57], v[40:41] op_sel_hi:[0,1]
	v_pk_fma_f32 v[34:35], v[54:55], v[36:37], v[34:35] op_sel_hi:[0,1,1]
	v_pk_add_f32 v[40:41], v[34:35], v[32:33]
	v_cvt_pk_f32_fp8_e32 v[34:35], v88
	v_cvt_pk_f32_fp8_e32 v[32:33], v89
	v_cvt_pk_f32_fp8_sdwa v[58:59], v88 src0_sel:WORD_1
	v_cvt_pk_f32_fp8_sdwa v[36:37], v89 src0_sel:WORD_1
	v_pk_mul_f32 v[34:35], v[56:57], v[34:35] op_sel_hi:[0,1]
	v_pk_fma_f32 v[32:33], v[54:55], v[32:33], v[34:35] op_sel_hi:[0,1,1]
	v_pk_add_f32 v[34:35], v[32:33], v[60:61]
	v_pk_mul_f32 v[32:33], v[56:57], v[58:59] op_sel_hi:[0,1]
	v_pk_fma_f32 v[32:33], v[54:55], v[36:37], v[32:33] op_sel_hi:[0,1,1]
	v_cvt_pk_f32_fp8_e32 v[58:59], v86
	v_pk_add_f32 v[36:37], v[32:33], v[30:31]
	v_cvt_pk_f32_fp8_e32 v[30:31], v87
	v_cvt_pk_f32_fp8_sdwa v[60:61], v86 src0_sel:WORD_1
	v_cvt_pk_f32_fp8_sdwa v[32:33], v87 src0_sel:WORD_1
	v_pk_mul_f32 v[58:59], v[56:57], v[58:59] op_sel_hi:[0,1]
	v_pk_fma_f32 v[30:31], v[54:55], v[30:31], v[58:59] op_sel_hi:[0,1,1]
	v_pk_mul_f32 v[58:59], v[56:57], v[60:61] op_sel_hi:[0,1]
	v_pk_fma_f32 v[32:33], v[54:55], v[32:33], v[58:59] op_sel_hi:[0,1,1]
	v_cvt_pk_f32_fp8_e32 v[60:61], v55
	v_pk_add_f32 v[30:31], v[30:31], v[66:67]
	v_pk_add_f32 v[32:33], v[32:33], v[22:23]
	v_cvt_pk_f32_fp8_e32 v[22:23], v85
	v_cvt_pk_f32_fp8_sdwa v[66:67], v55 src0_sel:WORD_1
	v_cvt_pk_f32_fp8_sdwa v[58:59], v85 src0_sel:WORD_1
	v_pk_mul_f32 v[60:61], v[56:57], v[60:61] op_sel_hi:[0,1]
	v_pk_fma_f32 v[22:23], v[54:55], v[22:23], v[60:61] op_sel_hi:[0,1,1]
	v_pk_mul_f32 v[60:61], v[56:57], v[66:67] op_sel_hi:[0,1]
	v_pk_fma_f32 v[54:55], v[54:55], v[58:59], v[60:61] op_sel_hi:[0,1,1]
	v_mov_b32_e32 v58, v63
	v_mov_b32_e32 v59, v51
	v_pk_add_f32 v[24:25], v[54:55], v[24:25]
	v_mov_b32_e32 v54, v62
	v_mov_b32_e32 v55, v50
	v_pk_mul_f32 v[58:59], v[58:59], v[58:59]
	v_mov_b32_e32 v60, v65
	v_mov_b32_e32 v61, v53
	v_pk_fma_f32 v[54:55], v[54:55], v[54:55], v[58:59]
	v_mov_b32_e32 v58, v64
	v_mov_b32_e32 v59, v52
	v_pk_mul_f32 v[60:61], v[60:61], v[60:61]
	v_mul_f32_e32 v56, v43, v43
	v_pk_fma_f32 v[58:59], v[58:59], v[58:59], v[60:61]
	v_mov_b32_e32 v60, v47
	v_mov_b32_e32 v61, v49
	v_pk_add_f32 v[54:55], v[54:55], v[58:59]
	v_mov_b32_e32 v58, v46
	v_mov_b32_e32 v59, v48
	v_pk_mul_f32 v[60:61], v[60:61], v[60:61]
	v_pk_add_f32 v[22:23], v[22:23], v[68:69]
	v_pk_fma_f32 v[58:59], v[58:59], v[58:59], v[60:61]
	v_pk_fma_f32 v[60:61], v[42:43], v[42:43], v[56:57] op_sel_hi:[1,1,0]
	v_mul_f32_e32 v56, v45, v45
	v_pk_add_f32 v[54:55], v[54:55], v[54:55] op_sel:[0,1] op_sel_hi:[1,0]
	v_pk_add_f32 v[58:59], v[58:59], v[58:59] op_sel:[0,1] op_sel_hi:[1,0]
	v_pk_fma_f32 v[66:67], v[44:45], v[44:45], v[56:57] op_sel_hi:[1,1,0]
	v_pk_mul_f32 v[68:69], v[38:39], v[38:39]
	v_pk_mul_f32 v[70:71], v[40:41], v[40:41]
	v_mov_b32_e32 v55, v68
	v_mov_b32_e32 v59, v69
	v_mov_b32_e32 v61, v70
	v_mov_b32_e32 v67, v71
	v_pk_add_f32 v[54:55], v[54:55], v[58:59]
	v_pk_add_f32 v[58:59], v[60:61], v[66:67]
	v_mov_b32_e32 v60, v35
	v_mov_b32_e32 v61, v37
	v_pk_add_f32 v[54:55], v[54:55], v[58:59]
	v_mov_b32_e32 v58, v34
	v_mov_b32_e32 v59, v36
	v_pk_mul_f32 v[60:61], v[60:61], v[60:61]
	v_mul_f32_e32 v56, v31, v31
	v_pk_fma_f32 v[58:59], v[58:59], v[58:59], v[60:61]
	v_pk_fma_f32 v[60:61], v[30:31], v[30:31], v[56:57] op_sel_hi:[1,1,0]
	v_mul_f32_e32 v56, v33, v33
	v_pk_add_f32 v[54:55], v[54:55], v[54:55] op_sel:[0,1] op_sel_hi:[1,0]
	v_pk_add_f32 v[58:59], v[58:59], v[58:59] op_sel:[0,1] op_sel_hi:[1,0]
	v_pk_fma_f32 v[66:67], v[32:33], v[32:33], v[56:57] op_sel_hi:[1,1,0]
	v_pk_mul_f32 v[68:69], v[22:23], v[22:23]
	v_pk_mul_f32 v[70:71], v[24:25], v[24:25]
	v_mov_b32_e32 v55, v68
	v_mov_b32_e32 v59, v69
	v_mov_b32_e32 v61, v70
	v_mov_b32_e32 v67, v71
	v_pk_add_f32 v[54:55], v[54:55], v[58:59]
	v_pk_add_f32 v[58:59], v[60:61], v[66:67]
	s_nop 0
	v_pk_add_f32 v[54:55], v[54:55], v[58:59]
	s_nop 0
	v_add_f32_e32 v54, v54, v55
	ds_bpermute_b32 v55, v3, v54
	s_waitcnt lgkmcnt(0)
; #define GAS __attribute__((address_space(1)))
; __device__ __forceinline__ unsigned pk2(float lo, float hi) { f32x2_m v = {lo, hi}; bf16x2_m b = __builtin_convertvector(v, bf16x2_m); return __builtin_bit_cast(unsigned, b); }
; template <int MODE, bool W8 = false>
; __device__ __forceinline__ void norm_rows(const Ctx& C, const void* src, bf16* xdst, const unsigned char* YS8, const int* srow, const float* gate, const float* gain, bf16* XN, float* outf, unsigned char* XN8 = nullptr) {
;     ...
;             float ss = 0.f;
; #pragma unroll
;             for (int j = 0; j < 8; ++j) ss += (v[q][j].x * v[q][j].x + v[q][j].y * v[q][j].y) + (v[q][j].z * v[q][j].z + v[q][j].w * v[q][j].w);
;             const float rstd = 1.0f / sqrtf(wave_sum(ss) * (1.0f / DM) + RMS_EPS);
;             if (MODE == 1) { GAS v2u* xo = (GAS v2u*)(xdst + (size_t)m * DM) + C.lane;
; #pragma unroll
;                 for (int j = 0; j < 8; ++j) { v2u w; w.x = pk2(v[q][j].x, v[q][j].y); w.y = pk2(v[q][j].z, v[q][j].w); xo[64 * j] = w; } }
;             const GAS f32x4* gg = (const GAS f32x4*)gain + C.lane;
;             if (MODE <= 1) { GAS v2u* o = (GAS v2u*)(XN + (size_t)m * DM) + C.lane;
; #pragma unroll
;                 for (int j = 0; j < 8; ++j) { const f32x4 g = gg[64 * j]; const f32x4 y = v[q][j] * rstd * g; v2u w; w.x = pk2(y.x, y.y); w.y = pk2(y.z, y.w); o[64 * j] = w;
;                     if constexpr (W8) ((GAS unsigned*)(XN8 + (size_t)m * DM) + C.lane)[64 * j] = pk4_fp8m(y.x * SXN, y.y * SXN, y.z * SXN, y.w * SXN); } }
	v_add_f32_e32 v54, v54, v55
	ds_bpermute_b32 v55, v57, v54
	s_waitcnt lgkmcnt(0)
	v_add_f32_e32 v54, v54, v55
	ds_bpermute_b32 v55, v81, v54
	s_waitcnt lgkmcnt(0)
	v_add_f32_e32 v54, v54, v55
	ds_bpermute_b32 v55, v82, v54
	s_waitcnt lgkmcnt(0)
	v_add_f32_e32 v54, v54, v55
	ds_bpermute_b32 v55, v83, v54
	s_waitcnt lgkmcnt(0)
	v_add_f32_e32 v54, v54, v55
	ds_bpermute_b32 v55, v84, v54
	s_waitcnt lgkmcnt(0)
	v_add_f32_e32 v54, v54, v55
	v_fmamk_f32 v54, v54, 0x3a000000, v212
	v_cmp_gt_f32_e32 vcc, s12, v54
	v_mul_f32_e32 v55, 0x4f800000, v54
	s_nop 0
	v_cndmask_b32_e32 v54, v54, v55, vcc
	v_sqrt_f32_e32 v55, v54
	s_nop 0
	v_add_u32_e32 v56, -1, v55
	v_fma_f32 v58, -v56, v55, v54
	v_cmp_ge_f32_e64 s[2:3], 0, v58
	v_add_u32_e32 v58, 1, v55
	s_nop 0
	v_cndmask_b32_e64 v56, v55, v56, s[2:3]
	v_fma_f32 v55, -v58, v55, v54
	v_cmp_lt_f32_e64 s[2:3], 0, v55
	s_nop 1
	v_cndmask_b32_e64 v55, v56, v58, s[2:3]
	v_mul_f32_e32 v56, 0x37800000, v55
	v_cndmask_b32_e32 v55, v55, v56, vcc
	v_cmp_class_f32_e32 vcc, v54, v211
	s_nop 1
	v_cndmask_b32_e32 v56, v55, v54, vcc
	v_cvt_pk_bf16_f32 v54, v62, v63
	v_cvt_pk_bf16_f32 v55, v64, v65
	global_store_dwordx2 v[26:27], v[54:55], off
	s_nop 1
	v_cvt_pk_bf16_f32 v54, v50, v51
	v_cvt_pk_bf16_f32 v55, v52, v53
	global_store_dwordx2 v[26:27], v[54:55], off offset:512
	s_nop 1
	v_cvt_pk_bf16_f32 v54, v46, v47
	v_cvt_pk_bf16_f32 v55, v48, v49
	global_store_dwordx2 v[26:27], v[54:55], off offset:1024
	s_nop 1
	v_cvt_pk_bf16_f32 v54, v42, v43
	v_cvt_pk_bf16_f32 v55, v44, v45
	global_store_dwordx2 v[26:27], v[54:55], off offset:1536
	s_nop 1
	v_cvt_pk_bf16_f32 v54, v38, v39
	v_cvt_pk_bf16_f32 v55, v40, v41
	global_store_dwordx2 v[26:27], v[54:55], off offset:2048
	s_nop 1
	v_cvt_pk_bf16_f32 v54, v34, v35
	v_cvt_pk_bf16_f32 v55, v36, v37
	global_store_dwordx2 v[26:27], v[54:55], off offset:2560
	s_nop 1
	v_cvt_pk_bf16_f32 v54, v30, v31
	v_cvt_pk_bf16_f32 v55, v32, v33
	global_store_dwordx2 v[26:27], v[54:55], off offset:3072
	s_nop 1
	v_cvt_pk_bf16_f32 v54, v22, v23
	v_cvt_pk_bf16_f32 v55, v24, v25
	global_store_dwordx2 v[26:27], v[54:55], off offset:3584
	s_nop 1
	v_div_scale_f32 v26, s[2:3], v56, v56, 1.0
	v_rcp_f32_e32 v27, v26
	s_nop 0
	v_fma_f32 v54, -v26, v27, 1.0
	v_fmac_f32_e32 v27, v54, v27
	v_div_scale_f32 v54, vcc, 1.0, v56, 1.0
	v_mul_f32_e32 v55, v54, v27
	v_fma_f32 v58, -v26, v55, v54
	v_fmac_f32_e32 v55, v58, v27
	v_fma_f32 v26, -v26, v55, v54
	v_div_fmas_f32 v26, v26, v27, v55
	v_div_fixup_f32 v26, v26, v56, 1.0
	v_pk_mul_f32 v[54:55], v[62:63], v[26:27] op_sel_hi:[1,0]
	v_pk_mul_f32 v[62:63], v[64:65], v[26:27] op_sel_hi:[1,0]
	v_add_co_u32_e32 v28, vcc, s16, v28
	v_pk_mul_f32 v[54:55], v[160:161], v[54:55]
	s_nop 0
	v_cvt_pk_bf16_f32 v58, v54, v55
	v_mul_f32_e32 v27, 0x42000000, v54
	v_mul_f32_e32 v55, 0x42000000, v55
	v_med3_f32 v54, v27, s33, v214
	v_med3_f32 v55, v55, s33, v214
	v_mov_b32_e32 v27, v2
	v_pk_mul_f32 v[60:61], v[162:163], v[62:63]
	v_cvt_pk_fp8_f32 v27, v54, v55
	v_cvt_pk_bf16_f32 v59, v60, v61
	v_addc_co_u32_e32 v29, vcc, 0, v29, vcc
	global_store_dwordx2 v[28:29], v[58:59], off
	s_nop 1
	v_mul_f32_e32 v56, 0x42000000, v60
	v_mul_f32_e32 v58, 0x42000000, v61
	v_med3_f32 v56, v56, s33, v214
	v_med3_f32 v58, v58, s33, v214
	v_cvt_pk_fp8_f32 v27, v56, v58 op_sel:[0,0,1]
	v_lshl_add_u64 v[54:55], s[4:5], 0, v[14:15]
	v_add_co_u32_e32 v54, vcc, s17, v54
	v_pk_mul_f32 v[50:51], v[50:51], v[26:27] op_sel_hi:[1,0]
	s_nop 0
	v_addc_co_u32_e32 v55, vcc, 0, v55, vcc
	global_store_dword v[54:55], v27, off
	s_nop 1
	v_pk_mul_f32 v[52:53], v[52:53], v[26:27] op_sel_hi:[1,0]
	v_lshl_add_u64 v[14:15], v[14:15], 0, s[18:19]
	v_pk_mul_f32 v[50:51], v[164:165], v[50:51]
	v_pk_mul_f32 v[52:53], v[166:167], v[52:53]
	v_cvt_pk_bf16_f32 v58, v50, v51
	v_mul_f32_e32 v27, 0x42000000, v50
	v_mul_f32_e32 v50, 0x42000000, v51
	v_cvt_pk_bf16_f32 v59, v52, v53
	v_mul_f32_e32 v51, 0x42000000, v52
	v_mul_f32_e32 v52, 0x42000000, v53
	v_med3_f32 v27, v27, s33, v214
	v_med3_f32 v50, v50, s33, v214
	v_mov_b32_e32 v53, v2
	v_cvt_pk_fp8_f32 v53, v27, v50
	v_med3_f32 v51, v51, s33, v214
	v_med3_f32 v52, v52, s33, v214
	global_store_dwordx2 v[28:29], v[58:59], off offset:512
	s_nop 1
	v_cvt_pk_fp8_f32 v53, v51, v52 op_sel:[0,0,1]
	v_pk_mul_f32 v[46:47], v[46:47], v[26:27] op_sel_hi:[1,0]
	v_pk_mul_f32 v[48:49], v[48:49], v[26:27] op_sel_hi:[1,0]
	global_store_dword v[54:55], v53, off offset:256
	s_nop 1
	v_pk_mul_f32 v[46:47], v[46:47], v[168:169]
	v_pk_mul_f32 v[48:49], v[48:49], v[170:171]
; #define GAS __attribute__((address_space(1)))
; __device__ __forceinline__ unsigned pk2(float lo, float hi) { f32x2_m v = {lo, hi}; bf16x2_m b = __builtin_convertvector(v, bf16x2_m); return __builtin_bit_cast(unsigned, b); }
; template <int MODE, bool W8 = false>
; __device__ __forceinline__ void norm_rows(const Ctx& C, const void* src, bf16* xdst, const unsigned char* YS8, const int* srow, const float* gate, const float* gain, bf16* XN, float* outf, unsigned char* XN8 = nullptr) {
;     ...
;     for (int m0 = C.gw; m0 < T; m0 += NR * C.NGW) {
;     ...
;             const GAS f32x4* gg = (const GAS f32x4*)gain + C.lane;
;             if (MODE <= 1) { GAS v2u* o = (GAS v2u*)(XN + (size_t)m * DM) + C.lane;
; #pragma unroll
;                 for (int j = 0; j < 8; ++j) { const f32x4 g = gg[64 * j]; const f32x4 y = v[q][j] * rstd * g; v2u w; w.x = pk2(y.x, y.y); w.y = pk2(y.z, y.w); o[64 * j] = w;
;                     if constexpr (W8) ((GAS unsigned*)(XN8 + (size_t)m * DM) + C.lane)[64 * j] = pk4_fp8m(y.x * SXN, y.y * SXN, y.z * SXN, y.w * SXN); } }
	v_cvt_pk_bf16_f32 v50, v46, v47
	v_mul_f32_e32 v27, 0x42000000, v46
	v_mul_f32_e32 v46, 0x42000000, v47
	v_cvt_pk_bf16_f32 v51, v48, v49
	v_mul_f32_e32 v47, 0x42000000, v48
	v_mul_f32_e32 v48, 0x42000000, v49
	v_med3_f32 v27, v27, s33, v214
	v_med3_f32 v46, v46, s33, v214
	v_mov_b32_e32 v49, v2
	v_cvt_pk_fp8_f32 v49, v27, v46
	v_med3_f32 v47, v47, s33, v214
	v_med3_f32 v48, v48, s33, v214
	global_store_dwordx2 v[28:29], v[50:51], off offset:1024
	s_nop 1
	v_cvt_pk_fp8_f32 v49, v47, v48 op_sel:[0,0,1]
	v_pk_mul_f32 v[42:43], v[42:43], v[26:27] op_sel_hi:[1,0]
	v_pk_mul_f32 v[44:45], v[44:45], v[26:27] op_sel_hi:[1,0]
	global_store_dword v[54:55], v49, off offset:512
	s_nop 1
	v_pk_mul_f32 v[42:43], v[42:43], v[172:173]
	v_pk_mul_f32 v[44:45], v[44:45], v[174:175]
	v_cvt_pk_bf16_f32 v46, v42, v43
	v_mul_f32_e32 v27, 0x42000000, v42
	v_mul_f32_e32 v42, 0x42000000, v43
	v_cvt_pk_bf16_f32 v47, v44, v45
	v_mul_f32_e32 v43, 0x42000000, v44
	v_mul_f32_e32 v44, 0x42000000, v45
	v_med3_f32 v27, v27, s33, v214
	v_med3_f32 v42, v42, s33, v214
	v_mov_b32_e32 v45, v2
	v_cvt_pk_fp8_f32 v45, v27, v42
	v_med3_f32 v43, v43, s33, v214
	v_med3_f32 v44, v44, s33, v214
	global_store_dwordx2 v[28:29], v[46:47], off offset:1536
	s_nop 1
	v_cvt_pk_fp8_f32 v45, v43, v44 op_sel:[0,0,1]
	v_pk_mul_f32 v[38:39], v[38:39], v[26:27] op_sel_hi:[1,0]
	v_pk_mul_f32 v[40:41], v[40:41], v[26:27] op_sel_hi:[1,0]
	global_store_dword v[54:55], v45, off offset:768
	s_nop 1
	v_pk_mul_f32 v[38:39], v[38:39], v[176:177]
	v_pk_mul_f32 v[40:41], v[40:41], v[178:179]
	v_cvt_pk_bf16_f32 v42, v38, v39
	v_mul_f32_e32 v27, 0x42000000, v38
	v_mul_f32_e32 v38, 0x42000000, v39
	v_cvt_pk_bf16_f32 v43, v40, v41
	v_mul_f32_e32 v39, 0x42000000, v40
	v_mul_f32_e32 v40, 0x42000000, v41
	v_med3_f32 v27, v27, s33, v214
	v_med3_f32 v38, v38, s33, v214
	v_mov_b32_e32 v41, v2
	v_cvt_pk_fp8_f32 v41, v27, v38
	v_med3_f32 v39, v39, s33, v214
	v_med3_f32 v40, v40, s33, v214
	global_store_dwordx2 v[28:29], v[42:43], off offset:2048
	s_nop 1
	v_cvt_pk_fp8_f32 v41, v39, v40 op_sel:[0,0,1]
	v_pk_mul_f32 v[34:35], v[34:35], v[26:27] op_sel_hi:[1,0]
	v_pk_mul_f32 v[36:37], v[36:37], v[26:27] op_sel_hi:[1,0]
	global_store_dword v[54:55], v41, off offset:1024
	s_nop 1
	v_pk_mul_f32 v[34:35], v[34:35], v[180:181]
	v_pk_mul_f32 v[36:37], v[36:37], v[182:183]
	v_cvt_pk_bf16_f32 v38, v34, v35
	v_mul_f32_e32 v27, 0x42000000, v34
	v_mul_f32_e32 v34, 0x42000000, v35
	v_cvt_pk_bf16_f32 v39, v36, v37
	v_mul_f32_e32 v35, 0x42000000, v36
	v_mul_f32_e32 v36, 0x42000000, v37
	v_med3_f32 v27, v27, s33, v214
	v_med3_f32 v34, v34, s33, v214
	v_mov_b32_e32 v37, v2
	v_cvt_pk_fp8_f32 v37, v27, v34
	v_med3_f32 v35, v35, s33, v214
	v_med3_f32 v36, v36, s33, v214
	global_store_dwordx2 v[28:29], v[38:39], off offset:2560
	s_nop 1
	v_cvt_pk_fp8_f32 v37, v35, v36 op_sel:[0,0,1]
	v_pk_mul_f32 v[30:31], v[30:31], v[26:27] op_sel_hi:[1,0]
	v_pk_mul_f32 v[32:33], v[32:33], v[26:27] op_sel_hi:[1,0]
	global_store_dword v[54:55], v37, off offset:1280
	s_nop 1
	v_pk_mul_f32 v[30:31], v[30:31], v[184:185]
	v_pk_mul_f32 v[32:33], v[32:33], v[186:187]
	v_cvt_pk_bf16_f32 v34, v30, v31
	v_mul_f32_e32 v27, 0x42000000, v30
	v_mul_f32_e32 v30, 0x42000000, v31
	v_cvt_pk_bf16_f32 v35, v32, v33
	v_mul_f32_e32 v31, 0x42000000, v32
	v_mul_f32_e32 v32, 0x42000000, v33
	v_med3_f32 v27, v27, s33, v214
	v_med3_f32 v30, v30, s33, v214
	v_mov_b32_e32 v33, v2
	v_cvt_pk_fp8_f32 v33, v27, v30
	v_med3_f32 v31, v31, s33, v214
	v_med3_f32 v32, v32, s33, v214
	global_store_dwordx2 v[28:29], v[34:35], off offset:3072
	s_nop 1
	v_cvt_pk_fp8_f32 v33, v31, v32 op_sel:[0,0,1]
	v_pk_mul_f32 v[22:23], v[22:23], v[26:27] op_sel_hi:[1,0]
	v_pk_mul_f32 v[24:25], v[24:25], v[26:27] op_sel_hi:[1,0]
	global_store_dword v[54:55], v33, off offset:1536
	s_nop 1
	v_pk_mul_f32 v[24:25], v[24:25], v[190:191]
	v_pk_mul_f32 v[22:23], v[22:23], v[188:189]
	v_cvt_pk_bf16_f32 v27, v24, v25
	v_cvt_pk_bf16_f32 v26, v22, v23
	v_mul_f32_e32 v22, 0x42000000, v22
	v_mul_f32_e32 v23, 0x42000000, v23
	global_store_dwordx2 v[28:29], v[26:27], off offset:3584
	s_nop 1
	v_med3_f32 v22, v22, s33, v214
	v_med3_f32 v23, v23, s33, v214
	v_mov_b32_e32 v26, v2
	v_cvt_pk_fp8_f32 v26, v22, v23
	v_mul_f32_e32 v24, 0x42000000, v24
	v_mul_f32_e32 v25, 0x42000000, v25
	v_med3_f32 v24, v24, s33, v214
	v_med3_f32 v25, v25, s33, v214
	v_cvt_pk_fp8_f32 v26, v24, v25 op_sel:[0,0,1]
	global_store_dword v[54:55], v26, off offset:1792
	s_nop 1
	s_cbranch_scc0 .LBB0_1326
